# select-sort phase: second-half query loads issued with the first half's (one exposed load latency less per 16-token group)
# speedup vs baseline: 1.0464x; 1.0014x over previous
.LBB0_1367:
	v_ashrrev_i32_e32 v47, 31, v46
	v_lshlrev_b64 v[0:1], 13, v[46:47]
	v_lshl_add_u64 v[50:51], v[40:41], 0, v[0:1]
	global_load_dwordx4 v[24:27], v[50:51], off
	v_add_co_u32_e32 v48, vcc, 0x1000, v50
	s_movk_i32 s24, 0x7f
	s_nop 0
	v_addc_co_u32_e32 v49, vcc, 0, v51, vcc
	global_load_dwordx4 v[28:31], v[48:49], off
	global_load_dwordx4 v[16:19], v[50:51], off offset:64
	global_load_dwordx4 v[20:23], v[48:49], off offset:64
	global_load_dwordx4 v[8:11], v[50:51], off offset:128
	global_load_dwordx4 v[12:15], v[48:49], off offset:128
	global_load_dwordx4 v[0:3], v[50:51], off offset:192
	global_load_dwordx4 v[4:7], v[48:49], off offset:192
	global_load_dwordx4 v[218:221], v[50:51], off offset:256
	global_load_dwordx4 v[222:225], v[48:49], off offset:256
	global_load_dwordx4 v[226:229], v[50:51], off offset:320
	global_load_dwordx4 v[230:233], v[48:49], off offset:320
	global_load_dwordx4 v[234:237], v[50:51], off offset:384
	global_load_dwordx4 v[238:241], v[48:49], off offset:384
	global_load_dwordx4 v[242:245], v[50:51], off offset:448
	global_load_dwordx4 v[246:249], v[48:49], off offset:448
	ds_read_b128 v[158:161], v33
	ds_read_b128 v[162:165], v33 offset:256
	s_waitcnt vmcnt(8) lgkmcnt(0)
	v_mfma_f32_16x16x32_bf16 v[166:169], v[158:161], v[24:27], 0
	v_mfma_f32_16x16x32_bf16 v[158:161], v[158:161], v[28:31], v[166:169]
	v_mfma_f32_16x16x32_bf16 v[158:161], v[162:165], v[24:27], v[158:161]
	ds_read_b128 v[162:165], v33 offset:64
	s_nop 4
	ds_read_b128 v[166:169], v33 offset:320
	s_waitcnt lgkmcnt(1)
	v_mfma_f32_16x16x32_bf16 v[158:161], v[162:165], v[16:19], v[158:161]
	v_mfma_f32_16x16x32_bf16 v[158:161], v[162:165], v[20:23], v[158:161]
	s_waitcnt lgkmcnt(0)
	v_mfma_f32_16x16x32_bf16 v[158:161], v[166:169], v[16:19], v[158:161]
	ds_read_b128 v[162:165], v33 offset:128
	ds_read_b128 v[166:169], v33 offset:384
	s_waitcnt lgkmcnt(1)
	v_mfma_f32_16x16x32_bf16 v[158:161], v[162:165], v[8:11], v[158:161]
	v_mfma_f32_16x16x32_bf16 v[158:161], v[162:165], v[12:15], v[158:161]
	s_waitcnt lgkmcnt(0)
	v_mfma_f32_16x16x32_bf16 v[158:161], v[166:169], v[8:11], v[158:161]
	ds_read_b128 v[162:165], v33 offset:192
	ds_read_b128 v[166:169], v33 offset:448
	s_waitcnt lgkmcnt(1)
	v_mfma_f32_16x16x32_bf16 v[158:161], v[162:165], v[0:3], v[158:161]
	v_mfma_f32_16x16x32_bf16 v[158:161], v[162:165], v[4:7], v[158:161]
	s_waitcnt lgkmcnt(0)
	v_mfma_f32_16x16x32_bf16 v[158:161], v[166:169], v[0:3], v[158:161]
	ds_read_b128 v[162:165], v33 offset:8448
	ds_read_b128 v[166:169], v33 offset:8704
	s_waitcnt lgkmcnt(1)
	v_mfma_f32_16x16x32_bf16 v[170:173], v[162:165], v[24:27], 0
	s_nop 3
	v_cmp_gt_i32_e32 vcc, 0, v158
	v_not_b32_e32 v157, v158
	v_or_b32_e32 v158, 0x80000000, v158
	v_mfma_f32_16x16x32_bf16 v[162:165], v[162:165], v[28:31], v[170:173]
	v_cndmask_b32_e32 v157, v158, v157, vcc
	v_cmp_gt_i32_e32 vcc, 0, v159
	v_not_b32_e32 v158, v159
	s_waitcnt lgkmcnt(0)
	v_mfma_f32_16x16x32_bf16 v[162:165], v[166:169], v[24:27], v[162:165]
	ds_read_b128 v[166:169], v33 offset:8512
	ds_read_b128 v[170:173], v33 offset:8768
	v_or_b32_e32 v159, 0x80000000, v159
	v_cndmask_b32_e32 v158, v159, v158, vcc
	s_waitcnt lgkmcnt(1)
	v_mfma_f32_16x16x32_bf16 v[162:165], v[166:169], v[16:19], v[162:165]
	v_cmp_gt_i32_e32 vcc, 0, v160
	v_not_b32_e32 v159, v160
	v_or_b32_e32 v160, 0x80000000, v160
	v_mfma_f32_16x16x32_bf16 v[162:165], v[166:169], v[20:23], v[162:165]
	v_cndmask_b32_e32 v159, v160, v159, vcc
	v_cmp_gt_i32_e32 vcc, 0, v161
	v_not_b32_e32 v160, v161
	s_waitcnt lgkmcnt(0)
	v_mfma_f32_16x16x32_bf16 v[162:165], v[170:173], v[16:19], v[162:165]
	ds_read_b128 v[166:169], v33 offset:8576
	ds_read_b128 v[170:173], v33 offset:8832
	v_or_b32_e32 v161, 0x80000000, v161
	v_cndmask_b32_e32 v160, v161, v160, vcc
	s_waitcnt lgkmcnt(1)
	v_mfma_f32_16x16x32_bf16 v[162:165], v[166:169], v[8:11], v[162:165]
	v_and_or_b32 v157, v157, s33, v58
	v_and_or_b32 v158, v158, s33, v59
	v_and_or_b32 v159, v159, s33, v60
	v_mfma_f32_16x16x32_bf16 v[162:165], v[166:169], v[12:15], v[162:165]
	v_and_or_b32 v160, v160, s33, v61
	s_waitcnt lgkmcnt(0)
	v_mfma_f32_16x16x32_bf16 v[162:165], v[170:173], v[8:11], v[162:165]
	ds_read_b128 v[166:169], v33 offset:8640
	ds_read_b128 v[170:173], v33 offset:8896
	s_waitcnt lgkmcnt(1)
	v_mfma_f32_16x16x32_bf16 v[162:165], v[166:169], v[0:3], v[162:165]
	v_mfma_f32_16x16x32_bf16 v[162:165], v[166:169], v[4:7], v[162:165]
	s_waitcnt lgkmcnt(0)
	v_mfma_f32_16x16x32_bf16 v[162:165], v[170:173], v[0:3], v[162:165]
	ds_read_b128 v[166:169], v33 offset:16896
	ds_read_b128 v[170:173], v33 offset:17152
	s_waitcnt lgkmcnt(1)
	v_mfma_f32_16x16x32_bf16 v[174:177], v[166:169], v[24:27], 0
	s_nop 3
	v_cmp_gt_i32_e32 vcc, 0, v162
	v_not_b32_e32 v161, v162
	v_or_b32_e32 v162, 0x80000000, v162
	v_mfma_f32_16x16x32_bf16 v[166:169], v[166:169], v[28:31], v[174:177]
	v_cndmask_b32_e32 v161, v162, v161, vcc
	v_cmp_gt_i32_e32 vcc, 0, v163
	v_not_b32_e32 v162, v163
	s_waitcnt lgkmcnt(0)
	v_mfma_f32_16x16x32_bf16 v[166:169], v[170:173], v[24:27], v[166:169]
	ds_read_b128 v[170:173], v33 offset:16960
	ds_read_b128 v[174:177], v33 offset:17216
	v_or_b32_e32 v163, 0x80000000, v163
	v_cndmask_b32_e32 v162, v163, v162, vcc
	s_waitcnt lgkmcnt(1)
	v_mfma_f32_16x16x32_bf16 v[166:169], v[170:173], v[16:19], v[166:169]
	v_cmp_gt_i32_e32 vcc, 0, v164
	v_not_b32_e32 v163, v164
	v_or_b32_e32 v164, 0x80000000, v164
	v_mfma_f32_16x16x32_bf16 v[166:169], v[170:173], v[20:23], v[166:169]
	v_cndmask_b32_e32 v163, v164, v163, vcc
	v_cmp_gt_i32_e32 vcc, 0, v165
	v_not_b32_e32 v164, v165
	s_waitcnt lgkmcnt(0)
	v_mfma_f32_16x16x32_bf16 v[166:169], v[174:177], v[16:19], v[166:169]
	ds_read_b128 v[170:173], v33 offset:17024
	ds_read_b128 v[174:177], v33 offset:17280
	v_or_b32_e32 v165, 0x80000000, v165
	v_cndmask_b32_e32 v164, v165, v164, vcc
	s_waitcnt lgkmcnt(1)
	v_mfma_f32_16x16x32_bf16 v[166:169], v[170:173], v[8:11], v[166:169]
	v_and_or_b32 v161, v161, s33, v62
	v_and_or_b32 v162, v162, s33, v63
	v_and_or_b32 v163, v163, s33, v64
	v_mfma_f32_16x16x32_bf16 v[166:169], v[170:173], v[12:15], v[166:169]
	v_and_or_b32 v164, v164, s33, v65
	s_waitcnt lgkmcnt(0)
	v_mfma_f32_16x16x32_bf16 v[166:169], v[174:177], v[8:11], v[166:169]
	ds_read_b128 v[170:173], v33 offset:17088
	ds_read_b128 v[174:177], v33 offset:17344
	s_waitcnt lgkmcnt(1)
	v_mfma_f32_16x16x32_bf16 v[166:169], v[170:173], v[0:3], v[166:169]
	v_mfma_f32_16x16x32_bf16 v[166:169], v[170:173], v[4:7], v[166:169]
	s_waitcnt lgkmcnt(0)
	v_mfma_f32_16x16x32_bf16 v[166:169], v[174:177], v[0:3], v[166:169]
	ds_read_b128 v[170:173], v33 offset:25344
	ds_read_b128 v[174:177], v33 offset:25600
	s_waitcnt lgkmcnt(1)
	v_mfma_f32_16x16x32_bf16 v[178:181], v[170:173], v[24:27], 0
	s_nop 3
	v_cmp_gt_i32_e32 vcc, 0, v166
	v_not_b32_e32 v165, v166
	v_or_b32_e32 v166, 0x80000000, v166
	v_mfma_f32_16x16x32_bf16 v[170:173], v[170:173], v[28:31], v[178:181]
	v_cndmask_b32_e32 v165, v166, v165, vcc
	v_cmp_gt_i32_e32 vcc, 0, v167
	v_not_b32_e32 v166, v167
	s_waitcnt lgkmcnt(0)
	v_mfma_f32_16x16x32_bf16 v[170:173], v[174:177], v[24:27], v[170:173]
	ds_read_b128 v[174:177], v33 offset:25408
	ds_read_b128 v[178:181], v33 offset:25664
	v_or_b32_e32 v167, 0x80000000, v167
	v_cndmask_b32_e32 v166, v167, v166, vcc
	s_waitcnt lgkmcnt(1)
	v_mfma_f32_16x16x32_bf16 v[170:173], v[174:177], v[16:19], v[170:173]
	v_cmp_gt_i32_e32 vcc, 0, v168
	v_not_b32_e32 v167, v168
	v_or_b32_e32 v168, 0x80000000, v168
	v_mfma_f32_16x16x32_bf16 v[170:173], v[174:177], v[20:23], v[170:173]
	v_cndmask_b32_e32 v167, v168, v167, vcc
	v_cmp_gt_i32_e32 vcc, 0, v169
	v_not_b32_e32 v168, v169
	s_waitcnt lgkmcnt(0)
	v_mfma_f32_16x16x32_bf16 v[170:173], v[178:181], v[16:19], v[170:173]
	ds_read_b128 v[174:177], v33 offset:25472
	ds_read_b128 v[178:181], v33 offset:25728
	v_or_b32_e32 v169, 0x80000000, v169
	v_cndmask_b32_e32 v168, v169, v168, vcc
	s_waitcnt lgkmcnt(1)
	v_mfma_f32_16x16x32_bf16 v[170:173], v[174:177], v[8:11], v[170:173]
	v_and_or_b32 v165, v165, s33, v66
	v_and_or_b32 v166, v166, s33, v67
	v_and_or_b32 v167, v167, s33, v68
	v_mfma_f32_16x16x32_bf16 v[170:173], v[174:177], v[12:15], v[170:173]
	v_and_or_b32 v168, v168, s33, v69
	s_waitcnt lgkmcnt(0)
	v_mfma_f32_16x16x32_bf16 v[170:173], v[178:181], v[8:11], v[170:173]
	ds_read_b128 v[174:177], v33 offset:25536
	ds_read_b128 v[178:181], v33 offset:25792
	s_waitcnt lgkmcnt(1)
	v_mfma_f32_16x16x32_bf16 v[170:173], v[174:177], v[0:3], v[170:173]
	v_mfma_f32_16x16x32_bf16 v[170:173], v[174:177], v[4:7], v[170:173]
	s_waitcnt lgkmcnt(0)
	v_mfma_f32_16x16x32_bf16 v[170:173], v[178:181], v[0:3], v[170:173]
	ds_read_b128 v[174:177], v33 offset:33792
	ds_read_b128 v[178:181], v33 offset:34048
	s_waitcnt lgkmcnt(1)
	v_mfma_f32_16x16x32_bf16 v[182:185], v[174:177], v[24:27], 0
	s_nop 3
	v_cmp_gt_i32_e32 vcc, 0, v170
	v_not_b32_e32 v169, v170
	v_or_b32_e32 v170, 0x80000000, v170
	v_mfma_f32_16x16x32_bf16 v[174:177], v[174:177], v[28:31], v[182:185]
	v_cndmask_b32_e32 v169, v170, v169, vcc
	v_cmp_gt_i32_e32 vcc, 0, v171
	v_not_b32_e32 v170, v171
	s_waitcnt lgkmcnt(0)
	v_mfma_f32_16x16x32_bf16 v[174:177], v[178:181], v[24:27], v[174:177]
	ds_read_b128 v[178:181], v33 offset:33856
	ds_read_b128 v[182:185], v33 offset:34112
	v_or_b32_e32 v171, 0x80000000, v171
	v_cndmask_b32_e32 v170, v171, v170, vcc
	s_waitcnt lgkmcnt(1)
	v_mfma_f32_16x16x32_bf16 v[174:177], v[178:181], v[16:19], v[174:177]
	v_cmp_gt_i32_e32 vcc, 0, v172
	v_not_b32_e32 v171, v172
	v_or_b32_e32 v172, 0x80000000, v172
	v_mfma_f32_16x16x32_bf16 v[174:177], v[178:181], v[20:23], v[174:177]
	v_cndmask_b32_e32 v171, v172, v171, vcc
	v_cmp_gt_i32_e32 vcc, 0, v173
	v_not_b32_e32 v172, v173
	s_waitcnt lgkmcnt(0)
	v_mfma_f32_16x16x32_bf16 v[174:177], v[182:185], v[16:19], v[174:177]
	ds_read_b128 v[178:181], v33 offset:33920
	ds_read_b128 v[182:185], v33 offset:34176
	v_or_b32_e32 v173, 0x80000000, v173
	v_cndmask_b32_e32 v172, v173, v172, vcc
	s_waitcnt lgkmcnt(1)
	v_mfma_f32_16x16x32_bf16 v[174:177], v[178:181], v[8:11], v[174:177]
	v_and_or_b32 v169, v169, s33, v70
	v_and_or_b32 v170, v170, s33, v71
	v_and_or_b32 v171, v171, s33, v72
	v_mfma_f32_16x16x32_bf16 v[174:177], v[178:181], v[12:15], v[174:177]
	v_and_or_b32 v172, v172, s33, v73
	s_waitcnt lgkmcnt(0)
	v_mfma_f32_16x16x32_bf16 v[174:177], v[182:185], v[8:11], v[174:177]
	ds_read_b128 v[178:181], v33 offset:33984
	ds_read_b128 v[182:185], v33 offset:34240
	s_waitcnt lgkmcnt(1)
	v_mfma_f32_16x16x32_bf16 v[174:177], v[178:181], v[0:3], v[174:177]
	v_mfma_f32_16x16x32_bf16 v[174:177], v[178:181], v[4:7], v[174:177]
	s_waitcnt lgkmcnt(0)
	v_mfma_f32_16x16x32_bf16 v[174:177], v[182:185], v[0:3], v[174:177]
	ds_read_b128 v[178:181], v33 offset:42240
	ds_read_b128 v[182:185], v33 offset:42496
	s_waitcnt lgkmcnt(1)
	v_mfma_f32_16x16x32_bf16 v[186:189], v[178:181], v[24:27], 0
	s_nop 3
	v_cmp_gt_i32_e32 vcc, 0, v174
	v_not_b32_e32 v173, v174
	v_or_b32_e32 v174, 0x80000000, v174
	v_mfma_f32_16x16x32_bf16 v[178:181], v[178:181], v[28:31], v[186:189]
	v_cndmask_b32_e32 v173, v174, v173, vcc
	v_cmp_gt_i32_e32 vcc, 0, v175
	v_not_b32_e32 v174, v175
	s_waitcnt lgkmcnt(0)
	v_mfma_f32_16x16x32_bf16 v[178:181], v[182:185], v[24:27], v[178:181]
	ds_read_b128 v[182:185], v33 offset:42304
	ds_read_b128 v[186:189], v33 offset:42560
	v_or_b32_e32 v175, 0x80000000, v175
	v_cndmask_b32_e32 v174, v175, v174, vcc
	s_waitcnt lgkmcnt(1)
	v_mfma_f32_16x16x32_bf16 v[178:181], v[182:185], v[16:19], v[178:181]
	v_cmp_gt_i32_e32 vcc, 0, v176
	v_not_b32_e32 v175, v176
	v_or_b32_e32 v176, 0x80000000, v176
	v_mfma_f32_16x16x32_bf16 v[178:181], v[182:185], v[20:23], v[178:181]
	v_cndmask_b32_e32 v175, v176, v175, vcc
	v_cmp_gt_i32_e32 vcc, 0, v177
	v_not_b32_e32 v176, v177
	s_waitcnt lgkmcnt(0)
	v_mfma_f32_16x16x32_bf16 v[178:181], v[186:189], v[16:19], v[178:181]
	ds_read_b128 v[182:185], v33 offset:42368
	ds_read_b128 v[186:189], v33 offset:42624
	v_or_b32_e32 v177, 0x80000000, v177
	v_cndmask_b32_e32 v176, v177, v176, vcc
	s_waitcnt lgkmcnt(1)
	v_mfma_f32_16x16x32_bf16 v[178:181], v[182:185], v[8:11], v[178:181]
	v_and_or_b32 v173, v173, s33, v74
	v_and_or_b32 v174, v174, s33, v75
	v_and_or_b32 v175, v175, s33, v76
	v_mfma_f32_16x16x32_bf16 v[178:181], v[182:185], v[12:15], v[178:181]
	v_and_or_b32 v176, v176, s33, v77
	s_waitcnt lgkmcnt(0)
	v_mfma_f32_16x16x32_bf16 v[178:181], v[186:189], v[8:11], v[178:181]
	ds_read_b128 v[182:185], v33 offset:42432
	ds_read_b128 v[186:189], v33 offset:42688
	s_waitcnt lgkmcnt(1)
	v_mfma_f32_16x16x32_bf16 v[178:181], v[182:185], v[0:3], v[178:181]
	v_mfma_f32_16x16x32_bf16 v[178:181], v[182:185], v[4:7], v[178:181]
	s_waitcnt lgkmcnt(0)
	v_mfma_f32_16x16x32_bf16 v[178:181], v[186:189], v[0:3], v[178:181]
	ds_read_b128 v[182:185], v33 offset:50688
	ds_read_b128 v[186:189], v33 offset:50944
	s_waitcnt lgkmcnt(1)
	v_mfma_f32_16x16x32_bf16 v[200:203], v[182:185], v[24:27], 0
	s_nop 3
	v_cmp_gt_i32_e32 vcc, 0, v178
	v_not_b32_e32 v177, v178
	v_or_b32_e32 v178, 0x80000000, v178
	v_mfma_f32_16x16x32_bf16 v[182:185], v[182:185], v[28:31], v[200:203]
	v_cndmask_b32_e32 v177, v178, v177, vcc
	v_cmp_gt_i32_e32 vcc, 0, v179
	v_not_b32_e32 v178, v179
	s_waitcnt lgkmcnt(0)
	v_mfma_f32_16x16x32_bf16 v[182:185], v[186:189], v[24:27], v[182:185]
	ds_read_b128 v[186:189], v33 offset:50752
	ds_read_b128 v[200:203], v33 offset:51008
	v_or_b32_e32 v179, 0x80000000, v179
	v_cndmask_b32_e32 v178, v179, v178, vcc
	s_waitcnt lgkmcnt(1)
	v_mfma_f32_16x16x32_bf16 v[182:185], v[186:189], v[16:19], v[182:185]
	v_cmp_gt_i32_e32 vcc, 0, v180
	v_not_b32_e32 v179, v180
	v_or_b32_e32 v180, 0x80000000, v180
	v_mfma_f32_16x16x32_bf16 v[182:185], v[186:189], v[20:23], v[182:185]
	v_cndmask_b32_e32 v179, v180, v179, vcc
	v_cmp_gt_i32_e32 vcc, 0, v181
	v_not_b32_e32 v180, v181
	s_waitcnt lgkmcnt(0)
	v_mfma_f32_16x16x32_bf16 v[182:185], v[200:203], v[16:19], v[182:185]
	ds_read_b128 v[186:189], v33 offset:50816
	ds_read_b128 v[200:203], v33 offset:51072
	v_or_b32_e32 v181, 0x80000000, v181
	v_cndmask_b32_e32 v180, v181, v180, vcc
	s_waitcnt lgkmcnt(1)
	v_mfma_f32_16x16x32_bf16 v[182:185], v[186:189], v[8:11], v[182:185]
	v_and_or_b32 v177, v177, s33, v78
	v_and_or_b32 v178, v178, s33, v79
	v_and_or_b32 v179, v179, s33, v80
	v_mfma_f32_16x16x32_bf16 v[182:185], v[186:189], v[12:15], v[182:185]
	v_and_or_b32 v180, v180, s33, v81
	s_waitcnt lgkmcnt(0)
	v_mfma_f32_16x16x32_bf16 v[182:185], v[200:203], v[8:11], v[182:185]
	ds_read_b128 v[186:189], v33 offset:50880
	ds_read_b128 v[200:203], v33 offset:51136
	s_waitcnt lgkmcnt(1)
	v_mfma_f32_16x16x32_bf16 v[182:185], v[186:189], v[0:3], v[182:185]
	v_mfma_f32_16x16x32_bf16 v[182:185], v[186:189], v[4:7], v[182:185]
	s_waitcnt lgkmcnt(0)
	v_mfma_f32_16x16x32_bf16 v[182:185], v[200:203], v[0:3], v[182:185]
	ds_read_b128 v[186:189], v33 offset:59136
	ds_read_b128 v[200:203], v33 offset:59392
	s_waitcnt lgkmcnt(1)
	v_mfma_f32_16x16x32_bf16 v[204:207], v[186:189], v[24:27], 0
	s_nop 3
	v_cmp_gt_i32_e32 vcc, 0, v182
	v_not_b32_e32 v181, v182
	v_or_b32_e32 v182, 0x80000000, v182
	v_mfma_f32_16x16x32_bf16 v[28:31], v[186:189], v[28:31], v[204:207]
	v_cndmask_b32_e32 v181, v182, v181, vcc
	v_cmp_gt_i32_e32 vcc, 0, v183
	v_not_b32_e32 v182, v183
	s_waitcnt lgkmcnt(0)
	v_mfma_f32_16x16x32_bf16 v[24:27], v[200:203], v[24:27], v[28:31]
	s_nop 2
	ds_read_b128 v[28:31], v33 offset:59200
	ds_read_b128 v[186:189], v33 offset:59456
	v_or_b32_e32 v183, 0x80000000, v183
	v_cndmask_b32_e32 v182, v183, v182, vcc
	s_waitcnt lgkmcnt(1)
	v_mfma_f32_16x16x32_bf16 v[24:27], v[28:31], v[16:19], v[24:27]
	v_cmp_gt_i32_e32 vcc, 0, v184
	v_not_b32_e32 v183, v184
	v_or_b32_e32 v184, 0x80000000, v184
	v_mfma_f32_16x16x32_bf16 v[20:23], v[28:31], v[20:23], v[24:27]
	v_cndmask_b32_e32 v183, v184, v183, vcc
	v_cmp_gt_i32_e32 vcc, 0, v185
	v_not_b32_e32 v184, v185
	s_waitcnt lgkmcnt(0)
	v_mfma_f32_16x16x32_bf16 v[16:19], v[186:189], v[16:19], v[20:23]
	s_nop 2
	ds_read_b128 v[20:23], v33 offset:59264
	ds_read_b128 v[24:27], v33 offset:59520
	v_or_b32_e32 v185, 0x80000000, v185
	v_cndmask_b32_e32 v184, v185, v184, vcc
	s_waitcnt lgkmcnt(1)
	v_mfma_f32_16x16x32_bf16 v[16:19], v[20:23], v[8:11], v[16:19]
	v_and_or_b32 v181, v181, s33, v82
	v_and_or_b32 v182, v182, s33, v83
	v_and_or_b32 v183, v183, s33, v84
	v_mfma_f32_16x16x32_bf16 v[12:15], v[20:23], v[12:15], v[16:19]
	v_and_or_b32 v184, v184, s33, v85
	v_max_u32_e32 v28, v173, v174
	v_min_u32_e32 v29, v173, v174
	s_waitcnt lgkmcnt(0)
	v_mfma_f32_16x16x32_bf16 v[8:11], v[24:27], v[8:11], v[12:15]
	s_nop 2
	ds_read_b128 v[12:15], v33 offset:59328
	ds_read_b128 v[16:19], v33 offset:59584
	v_max_u32_e32 v30, v176, v175
	v_min_u32_e32 v31, v176, v175
	s_waitcnt lgkmcnt(1)
	v_mfma_f32_16x16x32_bf16 v[8:11], v[12:15], v[0:3], v[8:11]
	v_mfma_f32_16x16x32_bf16 v[4:7], v[12:15], v[4:7], v[8:11]
	v_max_u32_e32 v12, v165, v166
	v_min_u32_e32 v13, v165, v166
	v_max_u32_e32 v14, v168, v167
	s_waitcnt lgkmcnt(0)
	v_mfma_f32_16x16x32_bf16 v[0:3], v[16:19], v[0:3], v[4:7]
	s_nop 1
	v_max_u32_e32 v8, v161, v162
	v_min_u32_e32 v9, v161, v162
	v_max_u32_e32 v10, v164, v163
	v_min_u32_e32 v5, v157, v158
	v_max_u32_e32 v6, v160, v159
	s_nop 0
	v_cmp_gt_i32_e32 vcc, 0, v0
	v_not_b32_e32 v4, v0
	v_or_b32_e32 v0, 0x80000000, v0
	v_cndmask_b32_e32 v0, v0, v4, vcc
	v_cmp_gt_i32_e32 vcc, 0, v1
	v_not_b32_e32 v4, v1
	v_or_b32_e32 v1, 0x80000000, v1
	v_cndmask_b32_e32 v1, v1, v4, vcc
	v_cmp_gt_i32_e32 vcc, 0, v2
	v_not_b32_e32 v4, v2
	v_or_b32_e32 v2, 0x80000000, v2
	v_cndmask_b32_e32 v2, v2, v4, vcc
	v_cmp_gt_i32_e32 vcc, 0, v3
	v_not_b32_e32 v4, v3
	v_or_b32_e32 v3, 0x80000000, v3
	v_cndmask_b32_e32 v3, v3, v4, vcc
	v_and_or_b32 v0, v0, s33, v86
	v_and_or_b32 v1, v1, s33, v87
	v_and_or_b32 v2, v2, s33, v88
	v_and_or_b32 v3, v3, s33, v89
	v_max_u32_e32 v4, v157, v158
	v_min_u32_e32 v7, v160, v159
	v_min_u32_e32 v11, v164, v163
	v_min_u32_e32 v15, v168, v167
	v_max_u32_e32 v16, v169, v170
	v_min_u32_e32 v17, v169, v170
	v_max_u32_e32 v18, v172, v171
	v_min_u32_e32 v19, v172, v171
	v_max_u32_e32 v157, v177, v178
	v_min_u32_e32 v158, v177, v178
	v_max_u32_e32 v159, v180, v179
	v_min_u32_e32 v160, v180, v179
	v_max_u32_e32 v161, v181, v182
	v_min_u32_e32 v162, v181, v182
	v_max_u32_e32 v163, v184, v183
	v_min_u32_e32 v164, v184, v183
	v_max_u32_e32 v165, v0, v1
	v_min_u32_e32 v0, v0, v1
	v_max_u32_e32 v1, v3, v2
	v_min_u32_e32 v2, v3, v2
	v_max_u32_e32 v20, v4, v7
	v_min_u32_e32 v4, v4, v7
	v_max_u32_e32 v7, v5, v6
	v_min_u32_e32 v5, v5, v6
	v_max_u32_e32 v6, v11, v8
	v_min_u32_e32 v8, v11, v8
	v_max_u32_e32 v11, v10, v9
	v_min_u32_e32 v9, v10, v9
	v_max_u32_e32 v10, v12, v15
	v_min_u32_e32 v12, v12, v15
	v_max_u32_e32 v15, v13, v14
	v_min_u32_e32 v13, v13, v14
	v_max_u32_e32 v14, v19, v16
	v_min_u32_e32 v16, v19, v16
	v_max_u32_e32 v19, v18, v17
	v_min_u32_e32 v17, v18, v17
	v_max_u32_e32 v3, v28, v31
	v_min_u32_e32 v28, v28, v31
	v_max_u32_e32 v31, v29, v30
	v_min_u32_e32 v29, v29, v30
	v_max_u32_e32 v30, v160, v157
	v_min_u32_e32 v157, v160, v157
	v_max_u32_e32 v160, v159, v158
	v_min_u32_e32 v158, v159, v158
	v_max_u32_e32 v159, v161, v164
	v_min_u32_e32 v161, v161, v164
	v_max_u32_e32 v164, v162, v163
	v_min_u32_e32 v162, v162, v163
	v_max_u32_e32 v163, v2, v165
	v_min_u32_e32 v2, v2, v165
	v_max_u32_e32 v165, v1, v0
	v_min_u32_e32 v0, v1, v0
	v_max_u32_e32 v18, v20, v7
	v_min_u32_e32 v7, v20, v7
	v_max_u32_e32 v20, v4, v5
	v_min_u32_e32 v4, v4, v5
	v_max_u32_e32 v5, v9, v8
	v_min_u32_e32 v8, v9, v8
	v_max_u32_e32 v9, v11, v6
	v_min_u32_e32 v6, v11, v6
	v_max_u32_e32 v11, v10, v15
	v_min_u32_e32 v10, v10, v15
	v_max_u32_e32 v15, v12, v13
	v_min_u32_e32 v12, v12, v13
	v_max_u32_e32 v13, v17, v16
	v_min_u32_e32 v16, v17, v16
	v_max_u32_e32 v17, v19, v14
	v_min_u32_e32 v14, v19, v14
	v_max_u32_e32 v1, v3, v31
	v_min_u32_e32 v3, v3, v31
	v_max_u32_e32 v31, v28, v29
	v_min_u32_e32 v28, v28, v29
	v_max_u32_e32 v29, v158, v157
	v_min_u32_e32 v157, v158, v157
	v_max_u32_e32 v158, v160, v30
	v_min_u32_e32 v30, v160, v30
	v_max_u32_e32 v160, v159, v164
	v_min_u32_e32 v159, v159, v164
	v_max_u32_e32 v164, v161, v162
	v_min_u32_e32 v161, v161, v162
	v_max_u32_e32 v162, v0, v2
	v_min_u32_e32 v0, v0, v2
	v_max_u32_e32 v2, v165, v163
	v_min_u32_e32 v163, v165, v163
	v_max_u32_e32 v19, v18, v8
	v_min_u32_e32 v8, v18, v8
	v_max_u32_e32 v18, v7, v5
	v_min_u32_e32 v5, v7, v5
	v_max_u32_e32 v7, v20, v6
	v_min_u32_e32 v6, v20, v6
	v_max_u32_e32 v20, v4, v9
	v_min_u32_e32 v4, v4, v9
	v_max_u32_e32 v9, v16, v11
	v_min_u32_e32 v11, v16, v11
	v_max_u32_e32 v16, v13, v10
	v_min_u32_e32 v10, v13, v10
	v_max_u32_e32 v13, v14, v15
	v_min_u32_e32 v14, v14, v15
	v_max_u32_e32 v15, v17, v12
	v_min_u32_e32 v12, v17, v12
	v_max_u32_e32 v165, v1, v157
	v_min_u32_e32 v1, v1, v157
	v_max_u32_e32 v157, v3, v29
	v_min_u32_e32 v3, v3, v29
	v_max_u32_e32 v29, v31, v30
	v_min_u32_e32 v30, v31, v30
	v_max_u32_e32 v31, v28, v158
	v_min_u32_e32 v28, v28, v158
	v_max_u32_e32 v158, v0, v160
	v_min_u32_e32 v0, v0, v160
	v_max_u32_e32 v160, v162, v159
	v_min_u32_e32 v159, v162, v159
	v_max_u32_e32 v162, v163, v164
	v_min_u32_e32 v163, v163, v164
	v_max_u32_e32 v164, v2, v161
	v_min_u32_e32 v2, v2, v161
	v_max_u32_e32 v17, v19, v7
	v_min_u32_e32 v7, v19, v7
	v_max_u32_e32 v19, v18, v20
	v_min_u32_e32 v18, v18, v20
	v_max_u32_e32 v20, v8, v6
	v_min_u32_e32 v6, v8, v6
	v_max_u32_e32 v8, v5, v4
	v_min_u32_e32 v4, v5, v4
	v_max_u32_e32 v5, v14, v11
	v_min_u32_e32 v11, v14, v11
	v_max_u32_e32 v14, v12, v10
	v_min_u32_e32 v10, v12, v10
	v_max_u32_e32 v12, v13, v9
	v_min_u32_e32 v9, v13, v9
	v_max_u32_e32 v13, v15, v16
	v_min_u32_e32 v15, v15, v16
	v_max_u32_e32 v161, v165, v29
	v_min_u32_e32 v29, v165, v29
	v_max_u32_e32 v165, v157, v31
	v_min_u32_e32 v31, v157, v31
	v_max_u32_e32 v157, v1, v30
	v_min_u32_e32 v1, v1, v30
	v_max_u32_e32 v30, v3, v28
	v_min_u32_e32 v3, v3, v28
	v_max_u32_e32 v28, v163, v0
	v_min_u32_e32 v0, v163, v0
	v_max_u32_e32 v163, v2, v159
	v_min_u32_e32 v2, v2, v159
	v_max_u32_e32 v159, v162, v158
	v_min_u32_e32 v158, v162, v158
	v_max_u32_e32 v162, v164, v160
	v_min_u32_e32 v160, v164, v160
	v_max_u32_e32 v16, v17, v19
	v_min_u32_e32 v17, v17, v19
	v_max_u32_e32 v19, v7, v18
	v_min_u32_e32 v7, v7, v18
	v_max_u32_e32 v18, v20, v8
	v_min_u32_e32 v8, v20, v8
	v_max_u32_e32 v20, v6, v4
	v_min_u32_e32 v4, v6, v4
	v_max_u32_e32 v6, v10, v11
	v_min_u32_e32 v10, v10, v11
	v_max_u32_e32 v11, v14, v5
	v_min_u32_e32 v5, v14, v5
	v_max_u32_e32 v14, v15, v9
	v_min_u32_e32 v9, v15, v9
	v_max_u32_e32 v15, v13, v12
	v_min_u32_e32 v12, v13, v12
	v_max_u32_e32 v164, v161, v165
	v_min_u32_e32 v161, v161, v165
	v_max_u32_e32 v165, v29, v31
	v_min_u32_e32 v29, v29, v31
	v_max_u32_e32 v31, v157, v30
	v_min_u32_e32 v30, v157, v30
	v_max_u32_e32 v157, v1, v3
	v_min_u32_e32 v1, v1, v3
	v_max_u32_e32 v3, v2, v0
	v_min_u32_e32 v0, v2, v0
	v_max_u32_e32 v2, v163, v28
	v_min_u32_e32 v28, v163, v28
	v_max_u32_e32 v163, v160, v158
	v_min_u32_e32 v158, v160, v158
	v_max_u32_e32 v160, v162, v159
	v_min_u32_e32 v159, v162, v159
	v_max_u32_e32 v13, v16, v10
	v_min_u32_e32 v10, v16, v10
	v_max_u32_e32 v16, v17, v6
	v_min_u32_e32 v6, v17, v6
	v_max_u32_e32 v17, v19, v5
	v_min_u32_e32 v5, v19, v5
	v_max_u32_e32 v19, v7, v11
	v_min_u32_e32 v7, v7, v11
	v_max_u32_e32 v11, v18, v9
	v_min_u32_e32 v9, v18, v9
	v_max_u32_e32 v18, v8, v14
	v_min_u32_e32 v8, v8, v14
	v_max_u32_e32 v14, v20, v12
	v_min_u32_e32 v12, v20, v12
	v_max_u32_e32 v20, v4, v15
	v_min_u32_e32 v4, v4, v15
	v_max_u32_e32 v162, v164, v0
	v_min_u32_e32 v0, v164, v0
	v_max_u32_e32 v164, v161, v3
	v_min_u32_e32 v3, v161, v3
	v_max_u32_e32 v161, v165, v28
	v_min_u32_e32 v28, v165, v28
	v_max_u32_e32 v165, v29, v2
	v_min_u32_e32 v2, v29, v2
	v_max_u32_e32 v29, v31, v158
	v_min_u32_e32 v31, v31, v158
	v_max_u32_e32 v158, v30, v163
	v_min_u32_e32 v30, v30, v163
	v_max_u32_e32 v163, v157, v159
	v_min_u32_e32 v157, v157, v159
	v_max_u32_e32 v159, v1, v160
	v_min_u32_e32 v1, v1, v160
	v_max_u32_e32 v15, v13, v11
	v_min_u32_e32 v11, v13, v11
	v_max_u32_e32 v13, v16, v18
	v_min_u32_e32 v16, v16, v18
	v_max_u32_e32 v18, v17, v14
	v_min_u32_e32 v14, v17, v14
	v_max_u32_e32 v17, v19, v20
	v_min_u32_e32 v19, v19, v20
	v_max_u32_e32 v20, v10, v9
	v_min_u32_e32 v9, v10, v9
	v_max_u32_e32 v10, v6, v8
	v_min_u32_e32 v6, v6, v8
	v_max_u32_e32 v8, v5, v12
	v_min_u32_e32 v5, v5, v12
	v_max_u32_e32 v12, v7, v4
	v_min_u32_e32 v4, v7, v4
	v_max_u32_e32 v160, v162, v29
	v_min_u32_e32 v29, v162, v29
	v_max_u32_e32 v162, v164, v158
	v_min_u32_e32 v158, v164, v158
	v_max_u32_e32 v164, v161, v163
	v_min_u32_e32 v161, v161, v163
	v_max_u32_e32 v163, v165, v159
	v_min_u32_e32 v159, v165, v159
	v_max_u32_e32 v165, v0, v31
	v_min_u32_e32 v0, v0, v31
	v_max_u32_e32 v31, v3, v30
	v_min_u32_e32 v3, v3, v30
	v_max_u32_e32 v30, v28, v157
	v_min_u32_e32 v28, v28, v157
	v_max_u32_e32 v157, v2, v1
	v_min_u32_e32 v1, v2, v1
	v_max_u32_e32 v7, v15, v18
	v_min_u32_e32 v15, v15, v18
	v_max_u32_e32 v18, v13, v17
	v_min_u32_e32 v13, v13, v17
	v_max_u32_e32 v17, v11, v14
	v_min_u32_e32 v11, v11, v14
	v_max_u32_e32 v14, v16, v19
	v_min_u32_e32 v16, v16, v19
	v_max_u32_e32 v19, v20, v8
	v_min_u32_e32 v8, v20, v8
	v_max_u32_e32 v20, v10, v12
	v_min_u32_e32 v10, v10, v12
	v_max_u32_e32 v12, v9, v5
	v_min_u32_e32 v5, v9, v5
	v_max_u32_e32 v9, v6, v4
	v_min_u32_e32 v4, v6, v4
	v_max_u32_e32 v2, v160, v164
	v_min_u32_e32 v160, v160, v164
	v_max_u32_e32 v164, v162, v163
	v_min_u32_e32 v162, v162, v163
	v_max_u32_e32 v163, v29, v161
	v_min_u32_e32 v29, v29, v161
	v_max_u32_e32 v161, v158, v159
	v_min_u32_e32 v158, v158, v159
	v_max_u32_e32 v159, v165, v30
	v_min_u32_e32 v30, v165, v30
	v_max_u32_e32 v165, v31, v157
	v_min_u32_e32 v31, v31, v157
	v_max_u32_e32 v157, v0, v28
	v_min_u32_e32 v0, v0, v28
	v_max_u32_e32 v28, v3, v1
	v_min_u32_e32 v1, v3, v1
	v_min_u32_e32 v6, v7, v18
	v_min_u32_e32 v21, v15, v13
	v_min_u32_e32 v22, v17, v14
	v_min_u32_e32 v23, v11, v16
	v_min_u32_e32 v24, v19, v20
	v_min_u32_e32 v25, v8, v10
	v_min_u32_e32 v26, v12, v9
	v_min_u32_e32 v27, v5, v4
	v_min_u32_e32 v3, v2, v164
	v_min_u32_e32 v166, v160, v162
	v_min_u32_e32 v167, v163, v161
	v_min_u32_e32 v168, v29, v158
	v_min_u32_e32 v169, v159, v165
	v_min_u32_e32 v170, v30, v31
	v_min_u32_e32 v171, v157, v28
	v_min_u32_e32 v172, v0, v1
	v_max3_u32 v7, v7, v18, v172
	v_max3_u32 v0, v6, v0, v1
	v_max3_u32 v1, v15, v13, v171
	v_max3_u32 v6, v21, v157, v28
	v_max3_u32 v13, v17, v14, v170
	v_max3_u32 v14, v22, v30, v31
	v_max3_u32 v11, v11, v16, v169
	v_max3_u32 v15, v23, v159, v165
	v_max3_u32 v16, v19, v20, v168
	v_max3_u32 v17, v24, v29, v158
	v_max3_u32 v8, v8, v10, v167
	v_max3_u32 v10, v25, v163, v161
	v_max3_u32 v9, v12, v9, v166
	v_max3_u32 v12, v26, v160, v162
	v_max3_u32 v3, v5, v4, v3
	v_max3_u32 v2, v27, v2, v164
	v_max_u32_e32 v4, v7, v16
	v_min_u32_e32 v5, v7, v16
	v_max_u32_e32 v7, v0, v17
	v_min_u32_e32 v0, v0, v17
	v_max_u32_e32 v16, v1, v8
	v_min_u32_e32 v1, v1, v8
	v_max_u32_e32 v8, v6, v10
	v_min_u32_e32 v6, v6, v10
	v_max_u32_e32 v10, v13, v9
	v_min_u32_e32 v9, v13, v9
	v_max_u32_e32 v13, v14, v12
	v_min_u32_e32 v12, v14, v12
	v_max_u32_e32 v14, v11, v3
	v_min_u32_e32 v3, v11, v3
	v_max_u32_e32 v11, v15, v2
	v_min_u32_e32 v2, v15, v2
	v_max_u32_e32 v15, v4, v10
	v_min_u32_e32 v4, v4, v10
	v_max_u32_e32 v10, v7, v13
	v_min_u32_e32 v7, v7, v13
	v_max_u32_e32 v13, v16, v14
	v_min_u32_e32 v14, v16, v14
	v_max_u32_e32 v16, v8, v11
	v_min_u32_e32 v8, v8, v11
	v_max_u32_e32 v11, v5, v9
	v_min_u32_e32 v5, v5, v9
	v_max_u32_e32 v9, v0, v12
	v_min_u32_e32 v0, v0, v12
	v_max_u32_e32 v12, v1, v3
	v_min_u32_e32 v1, v1, v3
	v_max_u32_e32 v3, v6, v2
	v_min_u32_e32 v2, v6, v2
	v_max_u32_e32 v6, v15, v13
	v_min_u32_e32 v13, v15, v13
	v_max_u32_e32 v15, v10, v16
	v_min_u32_e32 v10, v10, v16
	v_max_u32_e32 v16, v4, v14
	v_min_u32_e32 v4, v4, v14
	v_max_u32_e32 v14, v7, v8
	v_min_u32_e32 v7, v7, v8
	v_max_u32_e32 v8, v11, v12
	v_min_u32_e32 v11, v11, v12
	v_max_u32_e32 v12, v9, v3
	v_min_u32_e32 v3, v9, v3
	v_max_u32_e32 v9, v5, v1
	v_min_u32_e32 v1, v5, v1
	v_max_u32_e32 v5, v0, v2
	v_min_u32_e32 v0, v0, v2
	v_max_u32_e32 v2, v6, v15
	v_min_u32_e32 v6, v6, v15
	v_max_u32_e32 v15, v13, v10
	v_min_u32_e32 v10, v13, v10
	v_max_u32_e32 v13, v16, v14
	v_min_u32_e32 v14, v16, v14
	v_max_u32_e32 v16, v4, v7
	v_min_u32_e32 v4, v4, v7
	v_max_u32_e32 v7, v8, v12
	v_min_u32_e32 v8, v8, v12
	v_max_u32_e32 v12, v11, v3
	v_min_u32_e32 v3, v11, v3
	v_max_u32_e32 v11, v9, v5
	v_min_u32_e32 v5, v9, v5
	v_max_u32_e32 v9, v1, v0
	v_min_u32_e32 v0, v1, v0
	ds_bpermute_b32 v1, v55, v0
	ds_bpermute_b32 v17, v55, v9
	ds_bpermute_b32 v18, v55, v5
	ds_bpermute_b32 v19, v55, v11
	ds_bpermute_b32 v20, v55, v3
	ds_bpermute_b32 v21, v55, v12
	ds_bpermute_b32 v22, v55, v8
	ds_bpermute_b32 v23, v55, v7
	ds_bpermute_b32 v24, v55, v4
	ds_bpermute_b32 v25, v55, v16
	ds_bpermute_b32 v26, v55, v14
	ds_bpermute_b32 v27, v55, v13
	ds_bpermute_b32 v28, v55, v10
	ds_bpermute_b32 v29, v55, v15
	ds_bpermute_b32 v30, v55, v6
	ds_bpermute_b32 v31, v55, v2
	s_waitcnt lgkmcnt(14)
	v_max_u32_e32 v1, v2, v1
	v_max_u32_e32 v2, v6, v17
	s_waitcnt lgkmcnt(13)
	v_max_u32_e32 v6, v15, v18
	s_waitcnt lgkmcnt(12)
	v_max_u32_e32 v10, v10, v19
	s_waitcnt lgkmcnt(11)
	v_max_u32_e32 v13, v13, v20
	s_waitcnt lgkmcnt(10)
	v_max_u32_e32 v14, v14, v21
	s_waitcnt lgkmcnt(9)
	v_max_u32_e32 v15, v16, v22
	s_waitcnt lgkmcnt(8)
	v_max_u32_e32 v4, v4, v23
	s_waitcnt lgkmcnt(7)
	v_max_u32_e32 v7, v7, v24
	s_waitcnt lgkmcnt(6)
	v_max_u32_e32 v8, v8, v25
	s_waitcnt lgkmcnt(5)
	v_max_u32_e32 v12, v12, v26
	s_waitcnt lgkmcnt(4)
	v_max_u32_e32 v3, v3, v27
	s_waitcnt lgkmcnt(3)
	v_max_u32_e32 v11, v11, v28
	s_waitcnt lgkmcnt(2)
	v_max_u32_e32 v5, v5, v29
	s_waitcnt lgkmcnt(1)
	v_max_u32_e32 v9, v9, v30
	s_waitcnt lgkmcnt(0)
	v_max_u32_e32 v0, v0, v31
	v_max_u32_e32 v16, v1, v7
	v_min_u32_e32 v1, v1, v7
	v_max_u32_e32 v7, v2, v8
	v_min_u32_e32 v2, v2, v8
	v_max_u32_e32 v8, v6, v12
	v_min_u32_e32 v6, v6, v12
	v_max_u32_e32 v12, v10, v3
	v_min_u32_e32 v3, v10, v3
	v_max_u32_e32 v10, v13, v11
	v_min_u32_e32 v11, v13, v11
	v_max_u32_e32 v13, v14, v5
	v_min_u32_e32 v5, v14, v5
	v_max_u32_e32 v14, v15, v9
	v_min_u32_e32 v9, v15, v9
	v_max_u32_e32 v15, v4, v0
	v_min_u32_e32 v0, v4, v0
	v_max_u32_e32 v4, v16, v10
	v_min_u32_e32 v10, v16, v10
	v_max_u32_e32 v16, v7, v13
	v_min_u32_e32 v7, v7, v13
	v_max_u32_e32 v13, v8, v14
	v_min_u32_e32 v8, v8, v14
	v_max_u32_e32 v14, v12, v15
	v_min_u32_e32 v12, v12, v15
	v_max_u32_e32 v15, v1, v11
	v_min_u32_e32 v1, v1, v11
	v_max_u32_e32 v11, v2, v5
	v_min_u32_e32 v2, v2, v5
	v_max_u32_e32 v5, v6, v9
	v_min_u32_e32 v6, v6, v9
	v_max_u32_e32 v9, v3, v0
	v_min_u32_e32 v0, v3, v0
	v_max_u32_e32 v3, v4, v13
	v_min_u32_e32 v4, v4, v13
	v_max_u32_e32 v13, v16, v14
	v_min_u32_e32 v14, v16, v14
	v_max_u32_e32 v16, v10, v8
	v_min_u32_e32 v8, v10, v8
	v_max_u32_e32 v10, v7, v12
	v_min_u32_e32 v7, v7, v12
	v_max_u32_e32 v12, v15, v5
	v_min_u32_e32 v5, v15, v5
	v_max_u32_e32 v15, v11, v9
	v_min_u32_e32 v9, v11, v9
	v_max_u32_e32 v11, v1, v6
	v_min_u32_e32 v1, v1, v6
	v_max_u32_e32 v6, v2, v0
	v_min_u32_e32 v0, v2, v0
	v_max_u32_e32 v2, v3, v13
	v_min_u32_e32 v3, v3, v13
	v_max_u32_e32 v13, v4, v14
	v_min_u32_e32 v4, v4, v14
	v_max_u32_e32 v14, v16, v10
	v_min_u32_e32 v10, v16, v10
	v_max_u32_e32 v16, v8, v7
	v_min_u32_e32 v7, v8, v7
	v_max_u32_e32 v8, v12, v15
	v_min_u32_e32 v12, v12, v15
	v_max_u32_e32 v15, v5, v9
	v_min_u32_e32 v5, v5, v9
	v_max_u32_e32 v9, v11, v6
	v_min_u32_e32 v6, v11, v6
	v_max_u32_e32 v11, v1, v0
	v_min_u32_e32 v0, v1, v0
	ds_bpermute_b32 v1, v56, v0
	ds_bpermute_b32 v17, v56, v11
	ds_bpermute_b32 v18, v56, v6
	ds_bpermute_b32 v19, v56, v9
	ds_bpermute_b32 v20, v56, v5
	ds_bpermute_b32 v21, v56, v15
	ds_bpermute_b32 v22, v56, v12
	ds_bpermute_b32 v23, v56, v8
	ds_bpermute_b32 v24, v56, v7
	ds_bpermute_b32 v25, v56, v16
	ds_bpermute_b32 v26, v56, v10
	ds_bpermute_b32 v27, v56, v14
	ds_bpermute_b32 v28, v56, v4
	ds_bpermute_b32 v29, v56, v13
	ds_bpermute_b32 v30, v56, v3
	ds_bpermute_b32 v31, v56, v2
	s_waitcnt lgkmcnt(14)
	v_max_u32_e32 v1, v2, v1
	v_max_u32_e32 v2, v3, v17
	s_waitcnt lgkmcnt(13)
	v_max_u32_e32 v3, v13, v18
	s_waitcnt lgkmcnt(12)
	v_max_u32_e32 v4, v4, v19
	s_waitcnt lgkmcnt(11)
	v_max_u32_e32 v13, v14, v20
	s_waitcnt lgkmcnt(10)
	v_max_u32_e32 v10, v10, v21
	s_waitcnt lgkmcnt(9)
	v_max_u32_e32 v14, v16, v22
	s_waitcnt lgkmcnt(8)
	v_max_u32_e32 v7, v7, v23
	s_waitcnt lgkmcnt(7)
	v_max_u32_e32 v8, v8, v24
	s_waitcnt lgkmcnt(6)
	v_max_u32_e32 v12, v12, v25
	s_waitcnt lgkmcnt(5)
	v_max_u32_e32 v15, v15, v26
	s_waitcnt lgkmcnt(4)
	v_max_u32_e32 v5, v5, v27
	s_waitcnt lgkmcnt(3)
	v_max_u32_e32 v9, v9, v28
	s_waitcnt lgkmcnt(2)
	v_max_u32_e32 v6, v6, v29
	s_waitcnt lgkmcnt(1)
	v_max_u32_e32 v11, v11, v30
	s_waitcnt lgkmcnt(0)
	v_max_u32_e32 v0, v0, v31
	v_max_u32_e32 v16, v1, v8
	v_min_u32_e32 v1, v1, v8
	v_max_u32_e32 v8, v2, v12
	v_min_u32_e32 v2, v2, v12
	v_max_u32_e32 v12, v3, v15
	v_min_u32_e32 v3, v3, v15
	v_max_u32_e32 v15, v4, v5
	v_min_u32_e32 v4, v4, v5
	v_max_u32_e32 v5, v13, v9
	v_min_u32_e32 v9, v13, v9
	v_max_u32_e32 v13, v10, v6
	v_min_u32_e32 v6, v10, v6
	v_max_u32_e32 v10, v14, v11
	v_min_u32_e32 v11, v14, v11
	v_max_u32_e32 v14, v7, v0
	v_min_u32_e32 v0, v7, v0
	v_max_u32_e32 v7, v16, v5
	v_min_u32_e32 v5, v16, v5
	v_max_u32_e32 v16, v8, v13
	v_min_u32_e32 v8, v8, v13
	v_max_u32_e32 v13, v12, v10
	v_min_u32_e32 v10, v12, v10
	v_max_u32_e32 v12, v15, v14
	v_min_u32_e32 v14, v15, v14
	v_max_u32_e32 v15, v1, v9
	v_min_u32_e32 v1, v1, v9
	v_max_u32_e32 v9, v2, v6
	v_min_u32_e32 v2, v2, v6
	v_max_u32_e32 v6, v3, v11
	v_min_u32_e32 v3, v3, v11
	v_max_u32_e32 v11, v4, v0
	v_min_u32_e32 v0, v4, v0
	v_max_u32_e32 v4, v7, v13
	v_min_u32_e32 v7, v7, v13
	v_max_u32_e32 v13, v16, v12
	v_min_u32_e32 v12, v16, v12
	v_max_u32_e32 v16, v5, v10
	v_min_u32_e32 v5, v5, v10
	v_max_u32_e32 v10, v8, v14
	v_min_u32_e32 v8, v8, v14
	v_max_u32_e32 v14, v15, v6
	v_min_u32_e32 v6, v15, v6
	v_max_u32_e32 v15, v9, v11
	v_min_u32_e32 v9, v9, v11
	v_max_u32_e32 v11, v1, v3
	v_min_u32_e32 v1, v1, v3
	v_max_u32_e32 v3, v2, v0
	v_min_u32_e32 v0, v2, v0
	v_max_u32_e32 v166, v4, v13
	v_min_u32_e32 v165, v4, v13
	v_max_u32_e32 v164, v7, v12
	v_min_u32_e32 v162, v7, v12
	v_max_u32_e32 v163, v16, v10
	v_min_u32_e32 v160, v16, v10
	v_max_u32_e32 v161, v5, v8
	v_min_u32_e32 v157, v5, v8
	v_max_u32_e32 v158, v14, v15
	v_min_u32_e32 v159, v14, v15
	v_max_u32_e32 v169, v6, v9
	v_min_u32_e32 v170, v6, v9
	v_max_u32_e32 v171, v11, v3
	v_min_u32_e32 v172, v11, v3
	v_max_u32_e32 v167, v1, v0
	v_min_u32_e32 v168, v1, v0
	ds_read_b128 v[48:51], v90
	ds_read_b128 v[174:177], v91
	s_waitcnt vmcnt(7) lgkmcnt(1)
	v_mfma_f32_16x16x32_bf16 v[178:181], v[48:51], v[218:221], 0
	s_waitcnt vmcnt(6)
	v_mfma_f32_16x16x32_bf16 v[48:51], v[48:51], v[222:225], v[178:181]
	s_waitcnt lgkmcnt(0)
	v_mfma_f32_16x16x32_bf16 v[48:51], v[174:177], v[218:221], v[48:51]
	ds_read_b128 v[174:177], v92
	s_nop 2
	ds_read_b128 v[178:181], v93
	s_waitcnt vmcnt(5) lgkmcnt(1)
	v_mfma_f32_16x16x32_bf16 v[48:51], v[174:177], v[226:229], v[48:51]
	s_waitcnt vmcnt(4)
	v_mfma_f32_16x16x32_bf16 v[48:51], v[174:177], v[230:233], v[48:51]
	s_waitcnt lgkmcnt(0)
	v_mfma_f32_16x16x32_bf16 v[48:51], v[178:181], v[226:229], v[48:51]
	ds_read_b128 v[174:177], v94
	ds_read_b128 v[178:181], v95
	s_waitcnt vmcnt(3) lgkmcnt(1)
	v_mfma_f32_16x16x32_bf16 v[48:51], v[174:177], v[234:237], v[48:51]
	s_waitcnt vmcnt(2)
	v_mfma_f32_16x16x32_bf16 v[48:51], v[174:177], v[238:241], v[48:51]
	s_waitcnt lgkmcnt(0)
	v_mfma_f32_16x16x32_bf16 v[48:51], v[178:181], v[234:237], v[48:51]
	ds_read_b128 v[174:177], v96
	ds_read_b128 v[178:181], v97
	s_waitcnt vmcnt(1) lgkmcnt(1)
	v_mfma_f32_16x16x32_bf16 v[48:51], v[174:177], v[242:245], v[48:51]
	s_waitcnt vmcnt(0)
	v_mfma_f32_16x16x32_bf16 v[48:51], v[174:177], v[246:249], v[48:51]
	s_waitcnt lgkmcnt(0)
	v_mfma_f32_16x16x32_bf16 v[48:51], v[178:181], v[242:245], v[48:51]
	ds_read_b128 v[174:177], v98
	ds_read_b128 v[178:181], v99
	s_waitcnt lgkmcnt(1)
	v_mfma_f32_16x16x32_bf16 v[182:185], v[174:177], v[218:221], 0
	s_nop 3
	v_cmp_gt_i32_e32 vcc, 0, v48
	v_not_b32_e32 v173, v48
	v_or_b32_e32 v48, 0x80000000, v48
	v_mfma_f32_16x16x32_bf16 v[174:177], v[174:177], v[222:225], v[182:185]
	v_cndmask_b32_e32 v48, v48, v173, vcc
	v_cmp_gt_i32_e32 vcc, 0, v49
	v_not_b32_e32 v173, v49
	s_waitcnt lgkmcnt(0)
	v_mfma_f32_16x16x32_bf16 v[174:177], v[178:181], v[218:221], v[174:177]
	ds_read_b128 v[178:181], v100
	ds_read_b128 v[182:185], v101
	v_or_b32_e32 v49, 0x80000000, v49
	v_cndmask_b32_e32 v49, v49, v173, vcc
	s_waitcnt lgkmcnt(1)
	v_mfma_f32_16x16x32_bf16 v[174:177], v[178:181], v[226:229], v[174:177]
	v_cmp_gt_i32_e32 vcc, 0, v50
	v_not_b32_e32 v173, v50
	v_or_b32_e32 v50, 0x80000000, v50
	v_mfma_f32_16x16x32_bf16 v[174:177], v[178:181], v[230:233], v[174:177]
	v_cndmask_b32_e32 v50, v50, v173, vcc
	v_cmp_gt_i32_e32 vcc, 0, v51
	v_not_b32_e32 v173, v51
	s_waitcnt lgkmcnt(0)
	v_mfma_f32_16x16x32_bf16 v[174:177], v[182:185], v[226:229], v[174:177]
	ds_read_b128 v[178:181], v102
	ds_read_b128 v[182:185], v103
	v_or_b32_e32 v51, 0x80000000, v51
	v_cndmask_b32_e32 v51, v51, v173, vcc
	s_waitcnt lgkmcnt(1)
	v_mfma_f32_16x16x32_bf16 v[174:177], v[178:181], v[234:237], v[174:177]
	v_and_or_b32 v48, v48, s33, v58
	v_and_or_b32 v49, v49, s33, v59
	v_and_or_b32 v50, v50, s33, v60
	v_mfma_f32_16x16x32_bf16 v[174:177], v[178:181], v[238:241], v[174:177]
	v_and_or_b32 v51, v51, s33, v61
	s_waitcnt lgkmcnt(0)
	v_mfma_f32_16x16x32_bf16 v[174:177], v[182:185], v[234:237], v[174:177]
	ds_read_b128 v[178:181], v104
	ds_read_b128 v[182:185], v105
	s_waitcnt lgkmcnt(1)
	v_mfma_f32_16x16x32_bf16 v[174:177], v[178:181], v[242:245], v[174:177]
	v_mfma_f32_16x16x32_bf16 v[174:177], v[178:181], v[246:249], v[174:177]
	s_waitcnt lgkmcnt(0)
	v_mfma_f32_16x16x32_bf16 v[174:177], v[182:185], v[242:245], v[174:177]
	ds_read_b128 v[178:181], v106
	ds_read_b128 v[182:185], v107
	s_waitcnt lgkmcnt(1)
	v_mfma_f32_16x16x32_bf16 v[186:189], v[178:181], v[218:221], 0
	s_nop 3
	v_cmp_gt_i32_e32 vcc, 0, v174
	v_not_b32_e32 v173, v174
	v_or_b32_e32 v174, 0x80000000, v174
	v_mfma_f32_16x16x32_bf16 v[178:181], v[178:181], v[222:225], v[186:189]
	v_cndmask_b32_e32 v173, v174, v173, vcc
	v_cmp_gt_i32_e32 vcc, 0, v175
	v_not_b32_e32 v174, v175
	s_waitcnt lgkmcnt(0)
	v_mfma_f32_16x16x32_bf16 v[178:181], v[182:185], v[218:221], v[178:181]
	ds_read_b128 v[182:185], v108
	ds_read_b128 v[186:189], v109
	v_or_b32_e32 v175, 0x80000000, v175
	v_cndmask_b32_e32 v174, v175, v174, vcc
	s_waitcnt lgkmcnt(1)
	v_mfma_f32_16x16x32_bf16 v[178:181], v[182:185], v[226:229], v[178:181]
	v_cmp_gt_i32_e32 vcc, 0, v176
	v_not_b32_e32 v175, v176
	v_or_b32_e32 v176, 0x80000000, v176
	v_mfma_f32_16x16x32_bf16 v[178:181], v[182:185], v[230:233], v[178:181]
	v_cndmask_b32_e32 v175, v176, v175, vcc
	v_cmp_gt_i32_e32 vcc, 0, v177
	v_not_b32_e32 v176, v177
	s_waitcnt lgkmcnt(0)
	v_mfma_f32_16x16x32_bf16 v[178:181], v[186:189], v[226:229], v[178:181]
	ds_read_b128 v[182:185], v110
	ds_read_b128 v[186:189], v111
	v_or_b32_e32 v177, 0x80000000, v177
	v_cndmask_b32_e32 v176, v177, v176, vcc
	s_waitcnt lgkmcnt(1)
	v_mfma_f32_16x16x32_bf16 v[178:181], v[182:185], v[234:237], v[178:181]
	v_and_or_b32 v173, v173, s33, v62
	v_and_or_b32 v174, v174, s33, v63
	v_and_or_b32 v175, v175, s33, v64
	v_mfma_f32_16x16x32_bf16 v[178:181], v[182:185], v[238:241], v[178:181]
	v_and_or_b32 v176, v176, s33, v65
	s_waitcnt lgkmcnt(0)
	v_mfma_f32_16x16x32_bf16 v[178:181], v[186:189], v[234:237], v[178:181]
	ds_read_b128 v[182:185], v112
	ds_read_b128 v[186:189], v113
	s_waitcnt lgkmcnt(1)
	v_mfma_f32_16x16x32_bf16 v[178:181], v[182:185], v[242:245], v[178:181]
	v_mfma_f32_16x16x32_bf16 v[178:181], v[182:185], v[246:249], v[178:181]
	s_waitcnt lgkmcnt(0)
	v_mfma_f32_16x16x32_bf16 v[178:181], v[186:189], v[242:245], v[178:181]
	ds_read_b128 v[182:185], v114
	ds_read_b128 v[186:189], v115
	s_waitcnt lgkmcnt(1)
	v_mfma_f32_16x16x32_bf16 v[200:203], v[182:185], v[218:221], 0
	s_nop 3
	v_cmp_gt_i32_e32 vcc, 0, v178
	v_not_b32_e32 v177, v178
	v_or_b32_e32 v178, 0x80000000, v178
	v_mfma_f32_16x16x32_bf16 v[182:185], v[182:185], v[222:225], v[200:203]
	v_cndmask_b32_e32 v177, v178, v177, vcc
	v_cmp_gt_i32_e32 vcc, 0, v179
	v_not_b32_e32 v178, v179
	s_waitcnt lgkmcnt(0)
	v_mfma_f32_16x16x32_bf16 v[182:185], v[186:189], v[218:221], v[182:185]
	ds_read_b128 v[186:189], v116
	ds_read_b128 v[200:203], v117
	v_or_b32_e32 v179, 0x80000000, v179
	v_cndmask_b32_e32 v178, v179, v178, vcc
	s_waitcnt lgkmcnt(1)
	v_mfma_f32_16x16x32_bf16 v[182:185], v[186:189], v[226:229], v[182:185]
	v_cmp_gt_i32_e32 vcc, 0, v180
	v_not_b32_e32 v179, v180
	v_or_b32_e32 v180, 0x80000000, v180
	v_mfma_f32_16x16x32_bf16 v[182:185], v[186:189], v[230:233], v[182:185]
	v_cndmask_b32_e32 v179, v180, v179, vcc
	v_cmp_gt_i32_e32 vcc, 0, v181
	v_not_b32_e32 v180, v181
	s_waitcnt lgkmcnt(0)
	v_mfma_f32_16x16x32_bf16 v[182:185], v[200:203], v[226:229], v[182:185]
	ds_read_b128 v[186:189], v118
	ds_read_b128 v[200:203], v119
	v_or_b32_e32 v181, 0x80000000, v181
	v_cndmask_b32_e32 v180, v181, v180, vcc
	s_waitcnt lgkmcnt(1)
	v_mfma_f32_16x16x32_bf16 v[182:185], v[186:189], v[234:237], v[182:185]
	v_and_or_b32 v177, v177, s33, v66
	v_and_or_b32 v178, v178, s33, v67
	v_and_or_b32 v179, v179, s33, v68
	v_mfma_f32_16x16x32_bf16 v[182:185], v[186:189], v[238:241], v[182:185]
	v_and_or_b32 v180, v180, s33, v69
	s_waitcnt lgkmcnt(0)
	v_mfma_f32_16x16x32_bf16 v[182:185], v[200:203], v[234:237], v[182:185]
	ds_read_b128 v[186:189], v120
	ds_read_b128 v[200:203], v121
	s_waitcnt lgkmcnt(1)
	v_mfma_f32_16x16x32_bf16 v[182:185], v[186:189], v[242:245], v[182:185]
	v_mfma_f32_16x16x32_bf16 v[182:185], v[186:189], v[246:249], v[182:185]
	s_waitcnt lgkmcnt(0)
	v_mfma_f32_16x16x32_bf16 v[182:185], v[200:203], v[242:245], v[182:185]
	ds_read_b128 v[186:189], v122
	ds_read_b128 v[200:203], v123
	s_waitcnt lgkmcnt(1)
	v_mfma_f32_16x16x32_bf16 v[204:207], v[186:189], v[218:221], 0
	s_nop 3
	v_cmp_gt_i32_e32 vcc, 0, v182
	v_not_b32_e32 v181, v182
	v_or_b32_e32 v182, 0x80000000, v182
	v_mfma_f32_16x16x32_bf16 v[186:189], v[186:189], v[222:225], v[204:207]
	v_cndmask_b32_e32 v181, v182, v181, vcc
	v_cmp_gt_i32_e32 vcc, 0, v183
	v_not_b32_e32 v182, v183
	s_waitcnt lgkmcnt(0)
	v_mfma_f32_16x16x32_bf16 v[186:189], v[200:203], v[218:221], v[186:189]
	ds_read_b128 v[200:203], v124
	ds_read_b128 v[204:207], v125
	v_or_b32_e32 v183, 0x80000000, v183
	v_cndmask_b32_e32 v182, v183, v182, vcc
	s_waitcnt lgkmcnt(1)
	v_mfma_f32_16x16x32_bf16 v[186:189], v[200:203], v[226:229], v[186:189]
	v_cmp_gt_i32_e32 vcc, 0, v184
	v_not_b32_e32 v183, v184
	v_or_b32_e32 v184, 0x80000000, v184
	v_mfma_f32_16x16x32_bf16 v[186:189], v[200:203], v[230:233], v[186:189]
	v_cndmask_b32_e32 v183, v184, v183, vcc
	v_cmp_gt_i32_e32 vcc, 0, v185
	v_not_b32_e32 v184, v185
	s_waitcnt lgkmcnt(0)
	v_mfma_f32_16x16x32_bf16 v[186:189], v[204:207], v[226:229], v[186:189]
	ds_read_b128 v[200:203], v126
	ds_read_b128 v[204:207], v127
	v_or_b32_e32 v185, 0x80000000, v185
	v_cndmask_b32_e32 v184, v185, v184, vcc
	s_waitcnt lgkmcnt(1)
	v_mfma_f32_16x16x32_bf16 v[186:189], v[200:203], v[234:237], v[186:189]
	v_and_or_b32 v181, v181, s33, v70
	v_and_or_b32 v182, v182, s33, v71
	v_and_or_b32 v183, v183, s33, v72
	v_mfma_f32_16x16x32_bf16 v[186:189], v[200:203], v[238:241], v[186:189]
	v_and_or_b32 v184, v184, s33, v73
	s_waitcnt lgkmcnt(0)
	v_mfma_f32_16x16x32_bf16 v[186:189], v[204:207], v[234:237], v[186:189]
	ds_read_b128 v[200:203], v128
	ds_read_b128 v[204:207], v129
	s_waitcnt lgkmcnt(1)
	v_mfma_f32_16x16x32_bf16 v[186:189], v[200:203], v[242:245], v[186:189]
	v_mfma_f32_16x16x32_bf16 v[186:189], v[200:203], v[246:249], v[186:189]
	s_waitcnt lgkmcnt(0)
	v_mfma_f32_16x16x32_bf16 v[186:189], v[204:207], v[242:245], v[186:189]
	ds_read_b128 v[200:203], v130
	ds_read_b128 v[204:207], v131
	s_waitcnt lgkmcnt(1)
	v_mfma_f32_16x16x32_bf16 v[208:211], v[200:203], v[218:221], 0
	s_nop 3
	v_cmp_gt_i32_e32 vcc, 0, v186
	v_not_b32_e32 v185, v186
	v_or_b32_e32 v186, 0x80000000, v186
	v_mfma_f32_16x16x32_bf16 v[200:203], v[200:203], v[222:225], v[208:211]
	v_cndmask_b32_e32 v185, v186, v185, vcc
	v_cmp_gt_i32_e32 vcc, 0, v187
	v_not_b32_e32 v186, v187
	s_waitcnt lgkmcnt(0)
	v_mfma_f32_16x16x32_bf16 v[200:203], v[204:207], v[218:221], v[200:203]
	ds_read_b128 v[204:207], v132
	ds_read_b128 v[208:211], v133
	v_or_b32_e32 v187, 0x80000000, v187
	v_cndmask_b32_e32 v186, v187, v186, vcc
	s_waitcnt lgkmcnt(1)
	v_mfma_f32_16x16x32_bf16 v[200:203], v[204:207], v[226:229], v[200:203]
	v_cmp_gt_i32_e32 vcc, 0, v188
	v_not_b32_e32 v187, v188
	v_or_b32_e32 v188, 0x80000000, v188
	v_mfma_f32_16x16x32_bf16 v[200:203], v[204:207], v[230:233], v[200:203]
	v_cndmask_b32_e32 v187, v188, v187, vcc
	v_cmp_gt_i32_e32 vcc, 0, v189
	v_not_b32_e32 v188, v189
	s_waitcnt lgkmcnt(0)
	v_mfma_f32_16x16x32_bf16 v[200:203], v[208:211], v[226:229], v[200:203]
	ds_read_b128 v[204:207], v134
	ds_read_b128 v[208:211], v135
	v_or_b32_e32 v189, 0x80000000, v189
	v_cndmask_b32_e32 v188, v189, v188, vcc
	s_waitcnt lgkmcnt(1)
	v_mfma_f32_16x16x32_bf16 v[200:203], v[204:207], v[234:237], v[200:203]
	v_and_or_b32 v185, v185, s33, v74
	v_and_or_b32 v186, v186, s33, v75
	v_and_or_b32 v187, v187, s33, v76
	v_mfma_f32_16x16x32_bf16 v[200:203], v[204:207], v[238:241], v[200:203]
	v_and_or_b32 v188, v188, s33, v77
	s_waitcnt lgkmcnt(0)
	v_mfma_f32_16x16x32_bf16 v[200:203], v[208:211], v[234:237], v[200:203]
	ds_read_b128 v[204:207], v136
	ds_read_b128 v[208:211], v137
	s_waitcnt lgkmcnt(1)
	v_mfma_f32_16x16x32_bf16 v[200:203], v[204:207], v[242:245], v[200:203]
	v_mfma_f32_16x16x32_bf16 v[200:203], v[204:207], v[246:249], v[200:203]
	s_waitcnt lgkmcnt(0)
	v_mfma_f32_16x16x32_bf16 v[200:203], v[208:211], v[242:245], v[200:203]
	s_nop 7
	v_cmp_gt_i32_e32 vcc, 0, v200
	v_not_b32_e32 v189, v200
	v_or_b32_e32 v190, 0x80000000, v200
	v_cndmask_b32_e32 v189, v190, v189, vcc
	v_cmp_gt_i32_e32 vcc, 0, v201
	v_not_b32_e32 v190, v201
	v_or_b32_e32 v191, 0x80000000, v201
	v_cndmask_b32_e32 v190, v191, v190, vcc
	v_cmp_gt_i32_e32 vcc, 0, v202
	v_not_b32_e32 v191, v202
	v_or_b32_e32 v192, 0x80000000, v202
	v_cndmask_b32_e32 v191, v192, v191, vcc
	v_cmp_gt_i32_e32 vcc, 0, v203
	v_not_b32_e32 v192, v203
	v_or_b32_e32 v200, 0x80000000, v203
	v_cndmask_b32_e32 v192, v200, v192, vcc
	ds_read_b128 v[200:203], v138
	ds_read_b128 v[204:207], v139
	s_waitcnt lgkmcnt(1)
	v_mfma_f32_16x16x32_bf16 v[208:211], v[200:203], v[218:221], 0
	v_and_or_b32 v189, v189, s33, v78
	v_and_or_b32 v190, v190, s33, v79
	v_and_or_b32 v191, v191, s33, v80
	v_mfma_f32_16x16x32_bf16 v[200:203], v[200:203], v[222:225], v[208:211]
	v_and_or_b32 v192, v192, s33, v81
	s_waitcnt lgkmcnt(0)
	v_mfma_f32_16x16x32_bf16 v[200:203], v[204:207], v[218:221], v[200:203]
	ds_read_b128 v[204:207], v140
	ds_read_b128 v[208:211], v141
	s_waitcnt lgkmcnt(1)
	v_mfma_f32_16x16x32_bf16 v[200:203], v[204:207], v[226:229], v[200:203]
	v_mfma_f32_16x16x32_bf16 v[200:203], v[204:207], v[230:233], v[200:203]
	s_waitcnt lgkmcnt(0)
	v_mfma_f32_16x16x32_bf16 v[200:203], v[208:211], v[226:229], v[200:203]
	ds_read_b128 v[204:207], v142
	ds_read_b128 v[208:211], v143
	s_waitcnt lgkmcnt(1)
	v_mfma_f32_16x16x32_bf16 v[200:203], v[204:207], v[234:237], v[200:203]
	v_mfma_f32_16x16x32_bf16 v[200:203], v[204:207], v[238:241], v[200:203]
	s_waitcnt lgkmcnt(0)
	v_mfma_f32_16x16x32_bf16 v[200:203], v[208:211], v[234:237], v[200:203]
	ds_read_b128 v[204:207], v144
	ds_read_b128 v[208:211], v145
	s_waitcnt lgkmcnt(1)
	v_mfma_f32_16x16x32_bf16 v[200:203], v[204:207], v[242:245], v[200:203]
	v_mfma_f32_16x16x32_bf16 v[200:203], v[204:207], v[246:249], v[200:203]
	s_waitcnt lgkmcnt(0)
	v_mfma_f32_16x16x32_bf16 v[200:203], v[208:211], v[242:245], v[200:203]
	s_nop 7
	v_cmp_gt_i32_e32 vcc, 0, v200
	v_not_b32_e32 v204, v200
	v_or_b32_e32 v200, 0x80000000, v200
	v_cndmask_b32_e32 v200, v200, v204, vcc
	v_cmp_gt_i32_e32 vcc, 0, v201
	v_not_b32_e32 v204, v201
	v_or_b32_e32 v201, 0x80000000, v201
	v_cndmask_b32_e32 v201, v201, v204, vcc
	v_cmp_gt_i32_e32 vcc, 0, v202
	v_not_b32_e32 v204, v202
	v_or_b32_e32 v202, 0x80000000, v202
	v_cndmask_b32_e32 v202, v202, v204, vcc
	v_cmp_gt_i32_e32 vcc, 0, v203
	v_not_b32_e32 v204, v203
	v_or_b32_e32 v203, 0x80000000, v203
	v_cndmask_b32_e32 v203, v203, v204, vcc
	ds_read_b128 v[204:207], v146
	ds_read_b128 v[208:211], v147
	s_waitcnt lgkmcnt(1)
	v_mfma_f32_16x16x32_bf16 v[212:215], v[204:207], v[218:221], 0
	v_and_or_b32 v200, v200, s33, v82
	v_and_or_b32 v201, v201, s33, v83
	v_and_or_b32 v202, v202, s33, v84
	v_mfma_f32_16x16x32_bf16 v[28:31], v[204:207], v[222:225], v[212:215]
	v_and_or_b32 v203, v203, s33, v85
	s_waitcnt lgkmcnt(0)
	v_mfma_f32_16x16x32_bf16 v[16:19], v[208:211], v[218:221], v[28:31]
	s_nop 4
	ds_read_b128 v[28:31], v148
	ds_read_b128 v[204:207], v149
	s_waitcnt lgkmcnt(1)
	v_mfma_f32_16x16x32_bf16 v[16:19], v[28:31], v[226:229], v[16:19]
	v_mfma_f32_16x16x32_bf16 v[16:19], v[28:31], v[230:233], v[16:19]
	v_max_u32_e32 v28, v185, v186
	v_min_u32_e32 v29, v185, v186
	v_max_u32_e32 v30, v188, v187
	s_waitcnt lgkmcnt(0)
	v_mfma_f32_16x16x32_bf16 v[12:15], v[204:207], v[226:229], v[16:19]
	s_nop 2
	ds_read_b128 v[16:19], v150
	ds_read_b128 v[24:27], v151
	v_min_u32_e32 v31, v188, v187
	s_waitcnt lgkmcnt(1)
	v_mfma_f32_16x16x32_bf16 v[12:15], v[16:19], v[234:237], v[12:15]
	v_mfma_f32_16x16x32_bf16 v[12:15], v[16:19], v[238:241], v[12:15]
	s_waitcnt lgkmcnt(0)
	v_mfma_f32_16x16x32_bf16 v[8:11], v[24:27], v[234:237], v[12:15]
	s_nop 5
	ds_read_b128 v[12:15], v152
	ds_read_b128 v[16:19], v153
	s_waitcnt lgkmcnt(1)
	v_mfma_f32_16x16x32_bf16 v[8:11], v[12:15], v[242:245], v[8:11]
	v_mfma_f32_16x16x32_bf16 v[4:7], v[12:15], v[246:249], v[8:11]
	v_max_u32_e32 v12, v177, v178
	v_min_u32_e32 v13, v177, v178
	v_max_u32_e32 v14, v180, v179
	s_waitcnt lgkmcnt(0)
	v_mfma_f32_16x16x32_bf16 v[0:3], v[16:19], v[242:245], v[4:7]
	s_nop 1
	v_max_u32_e32 v8, v173, v174
	v_min_u32_e32 v9, v173, v174
	v_max_u32_e32 v10, v176, v175
	v_min_u32_e32 v5, v48, v49
	v_max_u32_e32 v6, v51, v50
	s_nop 0
	v_cmp_gt_i32_e32 vcc, 0, v0
	v_not_b32_e32 v4, v0
	v_or_b32_e32 v0, 0x80000000, v0
	v_cndmask_b32_e32 v0, v0, v4, vcc
	v_cmp_gt_i32_e32 vcc, 0, v1
	v_not_b32_e32 v4, v1
	v_or_b32_e32 v1, 0x80000000, v1
	v_cndmask_b32_e32 v1, v1, v4, vcc
	v_cmp_gt_i32_e32 vcc, 0, v2
	v_not_b32_e32 v4, v2
	v_or_b32_e32 v2, 0x80000000, v2
	v_cndmask_b32_e32 v2, v2, v4, vcc
	v_cmp_gt_i32_e32 vcc, 0, v3
	v_not_b32_e32 v4, v3
	v_or_b32_e32 v3, 0x80000000, v3
	v_cndmask_b32_e32 v3, v3, v4, vcc
	v_and_or_b32 v0, v0, s33, v86
	v_and_or_b32 v1, v1, s33, v87
	v_and_or_b32 v2, v2, s33, v88
	v_and_or_b32 v3, v3, s33, v89
	v_max_u32_e32 v4, v48, v49
	v_min_u32_e32 v7, v51, v50
	v_min_u32_e32 v11, v176, v175
	v_min_u32_e32 v15, v180, v179
	v_max_u32_e32 v16, v181, v182
	v_min_u32_e32 v17, v181, v182
	v_max_u32_e32 v18, v184, v183
	v_min_u32_e32 v19, v184, v183
	v_max_u32_e32 v48, v189, v190
	v_min_u32_e32 v49, v189, v190
	v_max_u32_e32 v50, v192, v191
	v_min_u32_e32 v51, v192, v191
	v_max_u32_e32 v173, v200, v201
	v_min_u32_e32 v174, v200, v201
	v_max_u32_e32 v175, v203, v202
	v_min_u32_e32 v176, v203, v202
	v_max_u32_e32 v177, v0, v1
	v_min_u32_e32 v0, v0, v1
	v_max_u32_e32 v1, v3, v2
	v_min_u32_e32 v2, v3, v2
	v_max_u32_e32 v20, v4, v7
	v_min_u32_e32 v4, v4, v7
	v_max_u32_e32 v7, v5, v6
	v_min_u32_e32 v5, v5, v6
	v_max_u32_e32 v6, v11, v8
	v_min_u32_e32 v8, v11, v8
	v_max_u32_e32 v11, v10, v9
	v_min_u32_e32 v9, v10, v9
	v_max_u32_e32 v10, v12, v15
	v_min_u32_e32 v12, v12, v15
	v_max_u32_e32 v15, v13, v14
	v_min_u32_e32 v13, v13, v14
	v_max_u32_e32 v14, v19, v16
	v_min_u32_e32 v16, v19, v16
	v_max_u32_e32 v19, v18, v17
	v_min_u32_e32 v17, v18, v17
	v_max_u32_e32 v3, v28, v31
	v_min_u32_e32 v28, v28, v31
	v_max_u32_e32 v31, v29, v30
	v_min_u32_e32 v29, v29, v30
	v_max_u32_e32 v30, v51, v48
	v_min_u32_e32 v48, v51, v48
	v_max_u32_e32 v51, v50, v49
	v_min_u32_e32 v49, v50, v49
	v_max_u32_e32 v50, v173, v176
	v_min_u32_e32 v173, v173, v176
	v_max_u32_e32 v176, v174, v175
	v_min_u32_e32 v174, v174, v175
	v_max_u32_e32 v175, v2, v177
	v_min_u32_e32 v2, v2, v177
	v_max_u32_e32 v177, v1, v0
	v_min_u32_e32 v0, v1, v0
	v_max_u32_e32 v18, v20, v7
	v_min_u32_e32 v7, v20, v7
	v_max_u32_e32 v20, v4, v5
	v_min_u32_e32 v4, v4, v5
	v_max_u32_e32 v5, v9, v8
	v_min_u32_e32 v8, v9, v8
	v_max_u32_e32 v9, v11, v6
	v_min_u32_e32 v6, v11, v6
	v_max_u32_e32 v11, v10, v15
	v_min_u32_e32 v10, v10, v15
	v_max_u32_e32 v15, v12, v13
	v_min_u32_e32 v12, v12, v13
	v_max_u32_e32 v13, v17, v16
	v_min_u32_e32 v16, v17, v16
	v_max_u32_e32 v17, v19, v14
	v_min_u32_e32 v14, v19, v14
	v_max_u32_e32 v1, v3, v31
	v_min_u32_e32 v3, v3, v31
	v_max_u32_e32 v31, v28, v29
	v_min_u32_e32 v28, v28, v29
	v_max_u32_e32 v29, v49, v48
	v_min_u32_e32 v48, v49, v48
	v_max_u32_e32 v49, v51, v30
	v_min_u32_e32 v30, v51, v30
	v_max_u32_e32 v51, v50, v176
	v_min_u32_e32 v50, v50, v176
	v_max_u32_e32 v176, v173, v174
	v_min_u32_e32 v173, v173, v174
	v_max_u32_e32 v174, v0, v2
	v_min_u32_e32 v0, v0, v2
	v_max_u32_e32 v2, v177, v175
	v_min_u32_e32 v175, v177, v175
	v_max_u32_e32 v19, v18, v8
	v_min_u32_e32 v8, v18, v8
	v_max_u32_e32 v18, v7, v5
	v_min_u32_e32 v5, v7, v5
	v_max_u32_e32 v7, v20, v6
	v_min_u32_e32 v6, v20, v6
	v_max_u32_e32 v20, v4, v9
	v_min_u32_e32 v4, v4, v9
	v_max_u32_e32 v9, v16, v11
	v_min_u32_e32 v11, v16, v11
	v_max_u32_e32 v16, v13, v10
	v_min_u32_e32 v10, v13, v10
	v_max_u32_e32 v13, v14, v15
	v_min_u32_e32 v14, v14, v15
	v_max_u32_e32 v15, v17, v12
	v_min_u32_e32 v12, v17, v12
	v_max_u32_e32 v177, v1, v48
	v_min_u32_e32 v1, v1, v48
	v_max_u32_e32 v48, v3, v29
	v_min_u32_e32 v3, v3, v29
	v_max_u32_e32 v29, v31, v30
	v_min_u32_e32 v30, v31, v30
	v_max_u32_e32 v31, v28, v49
	v_min_u32_e32 v28, v28, v49
	v_max_u32_e32 v49, v0, v51
	v_min_u32_e32 v0, v0, v51
	v_max_u32_e32 v51, v174, v50
	v_min_u32_e32 v50, v174, v50
	v_max_u32_e32 v174, v175, v176
	v_min_u32_e32 v175, v175, v176
	v_max_u32_e32 v176, v2, v173
	v_min_u32_e32 v2, v2, v173
	v_max_u32_e32 v17, v19, v7
	v_min_u32_e32 v7, v19, v7
	v_max_u32_e32 v19, v18, v20
	v_min_u32_e32 v18, v18, v20
	v_max_u32_e32 v20, v8, v6
	v_min_u32_e32 v6, v8, v6
	v_max_u32_e32 v8, v5, v4
	v_min_u32_e32 v4, v5, v4
	v_max_u32_e32 v5, v14, v11
	v_min_u32_e32 v11, v14, v11
	v_max_u32_e32 v14, v12, v10
	v_min_u32_e32 v10, v12, v10
	v_max_u32_e32 v12, v13, v9
	v_min_u32_e32 v9, v13, v9
	v_max_u32_e32 v13, v15, v16
	v_min_u32_e32 v15, v15, v16
	v_max_u32_e32 v173, v177, v29
	v_min_u32_e32 v29, v177, v29
	v_max_u32_e32 v177, v48, v31
	v_min_u32_e32 v31, v48, v31
	v_max_u32_e32 v48, v1, v30
	v_min_u32_e32 v1, v1, v30
	v_max_u32_e32 v30, v3, v28
	v_min_u32_e32 v3, v3, v28
	v_max_u32_e32 v28, v175, v0
	v_min_u32_e32 v0, v175, v0
	v_max_u32_e32 v175, v2, v50
	v_min_u32_e32 v2, v2, v50
	v_max_u32_e32 v50, v174, v49
	v_min_u32_e32 v49, v174, v49
	v_max_u32_e32 v174, v176, v51
	v_min_u32_e32 v51, v176, v51
	v_max_u32_e32 v16, v17, v19
	v_min_u32_e32 v17, v17, v19
	v_max_u32_e32 v19, v7, v18
	v_min_u32_e32 v7, v7, v18
	v_max_u32_e32 v18, v20, v8
	v_min_u32_e32 v8, v20, v8
	v_max_u32_e32 v20, v6, v4
	v_min_u32_e32 v4, v6, v4
	v_max_u32_e32 v6, v10, v11
	v_min_u32_e32 v10, v10, v11
	v_max_u32_e32 v11, v14, v5
	v_min_u32_e32 v5, v14, v5
	v_max_u32_e32 v14, v15, v9
	v_min_u32_e32 v9, v15, v9
	v_max_u32_e32 v15, v13, v12
	v_min_u32_e32 v12, v13, v12
	v_max_u32_e32 v176, v173, v177
	v_min_u32_e32 v173, v173, v177
	v_max_u32_e32 v177, v29, v31
	v_min_u32_e32 v29, v29, v31
	v_max_u32_e32 v31, v48, v30
	v_min_u32_e32 v30, v48, v30
	v_max_u32_e32 v48, v1, v3
	v_min_u32_e32 v1, v1, v3
	v_max_u32_e32 v3, v2, v0
	v_min_u32_e32 v0, v2, v0
	v_max_u32_e32 v2, v175, v28
	v_min_u32_e32 v28, v175, v28
	v_max_u32_e32 v175, v51, v49
	v_min_u32_e32 v49, v51, v49
	v_max_u32_e32 v51, v174, v50
	v_min_u32_e32 v50, v174, v50
	v_max_u32_e32 v13, v16, v10
	v_min_u32_e32 v10, v16, v10
	v_max_u32_e32 v16, v17, v6
	v_min_u32_e32 v6, v17, v6
	v_max_u32_e32 v17, v19, v5
	v_min_u32_e32 v5, v19, v5
	v_max_u32_e32 v19, v7, v11
	v_min_u32_e32 v7, v7, v11
	v_max_u32_e32 v11, v18, v9
	v_min_u32_e32 v9, v18, v9
	v_max_u32_e32 v18, v8, v14
	v_min_u32_e32 v8, v8, v14
	v_max_u32_e32 v14, v20, v12
	v_min_u32_e32 v12, v20, v12
	v_max_u32_e32 v20, v4, v15
	v_min_u32_e32 v4, v4, v15
	v_max_u32_e32 v174, v176, v0
	v_min_u32_e32 v0, v176, v0
	v_max_u32_e32 v176, v173, v3
	v_min_u32_e32 v3, v173, v3
	v_max_u32_e32 v173, v177, v28
	v_min_u32_e32 v28, v177, v28
	v_max_u32_e32 v177, v29, v2
	v_min_u32_e32 v2, v29, v2
	v_max_u32_e32 v29, v31, v49
	v_min_u32_e32 v31, v31, v49
	v_max_u32_e32 v49, v30, v175
	v_min_u32_e32 v30, v30, v175
	v_max_u32_e32 v175, v48, v50
	v_min_u32_e32 v48, v48, v50
	v_max_u32_e32 v50, v1, v51
	v_min_u32_e32 v1, v1, v51
	v_max_u32_e32 v15, v13, v11
	v_min_u32_e32 v11, v13, v11
	v_max_u32_e32 v13, v16, v18
	v_min_u32_e32 v16, v16, v18
	v_max_u32_e32 v18, v17, v14
	v_min_u32_e32 v14, v17, v14
	v_max_u32_e32 v17, v19, v20
	v_min_u32_e32 v19, v19, v20
	v_max_u32_e32 v20, v10, v9
	v_min_u32_e32 v9, v10, v9
	v_max_u32_e32 v10, v6, v8
	v_min_u32_e32 v6, v6, v8
	v_max_u32_e32 v8, v5, v12
	v_min_u32_e32 v5, v5, v12
	v_max_u32_e32 v12, v7, v4
	v_min_u32_e32 v4, v7, v4
	v_max_u32_e32 v51, v174, v29
	v_min_u32_e32 v29, v174, v29
	v_max_u32_e32 v174, v176, v49
	v_min_u32_e32 v49, v176, v49
	v_max_u32_e32 v176, v173, v175
	v_min_u32_e32 v173, v173, v175
	v_max_u32_e32 v175, v177, v50
	v_min_u32_e32 v50, v177, v50
	v_max_u32_e32 v177, v0, v31
	v_min_u32_e32 v0, v0, v31
	v_max_u32_e32 v31, v3, v30
	v_min_u32_e32 v3, v3, v30
	v_max_u32_e32 v30, v28, v48
	v_min_u32_e32 v28, v28, v48
	v_max_u32_e32 v48, v2, v1
	v_min_u32_e32 v1, v2, v1
	v_max_u32_e32 v7, v15, v18
	v_min_u32_e32 v15, v15, v18
	v_max_u32_e32 v18, v13, v17
	v_min_u32_e32 v13, v13, v17
	v_max_u32_e32 v17, v11, v14
	v_min_u32_e32 v11, v11, v14
	v_max_u32_e32 v14, v16, v19
	v_min_u32_e32 v16, v16, v19
	v_max_u32_e32 v19, v20, v8
	v_min_u32_e32 v8, v20, v8
	v_max_u32_e32 v20, v10, v12
	v_min_u32_e32 v10, v10, v12
	v_max_u32_e32 v12, v9, v5
	v_min_u32_e32 v5, v9, v5
	v_max_u32_e32 v9, v6, v4
	v_min_u32_e32 v4, v6, v4
	v_max_u32_e32 v2, v51, v176
	v_min_u32_e32 v51, v51, v176
	v_max_u32_e32 v176, v174, v175
	v_min_u32_e32 v174, v174, v175
	v_max_u32_e32 v175, v29, v173
	v_min_u32_e32 v29, v29, v173
	v_max_u32_e32 v173, v49, v50
	v_min_u32_e32 v49, v49, v50
	v_max_u32_e32 v50, v177, v30
	v_min_u32_e32 v30, v177, v30
	v_max_u32_e32 v177, v31, v48
	v_min_u32_e32 v31, v31, v48
	v_max_u32_e32 v48, v0, v28
	v_min_u32_e32 v0, v0, v28
	v_max_u32_e32 v28, v3, v1
	v_min_u32_e32 v1, v3, v1
	v_min_u32_e32 v6, v7, v18
	v_min_u32_e32 v21, v15, v13
	v_min_u32_e32 v22, v17, v14
	v_min_u32_e32 v23, v11, v16
	v_min_u32_e32 v24, v19, v20
	v_min_u32_e32 v25, v8, v10
	v_min_u32_e32 v26, v12, v9
	v_min_u32_e32 v27, v5, v4
	v_min_u32_e32 v3, v2, v176
	v_min_u32_e32 v178, v51, v174
	v_min_u32_e32 v179, v175, v173
	v_min_u32_e32 v180, v29, v49
	v_min_u32_e32 v181, v50, v177
	v_min_u32_e32 v182, v30, v31
	v_min_u32_e32 v183, v48, v28
	v_min_u32_e32 v184, v0, v1
	v_max3_u32 v7, v7, v18, v184
	v_max3_u32 v0, v6, v0, v1
	v_max3_u32 v1, v15, v13, v183
	v_max3_u32 v6, v21, v48, v28
	v_max3_u32 v13, v17, v14, v182
	v_max3_u32 v14, v22, v30, v31
	v_max3_u32 v11, v11, v16, v181
	v_max3_u32 v15, v23, v50, v177
	v_max3_u32 v16, v19, v20, v180
	v_max3_u32 v17, v24, v29, v49
	v_max3_u32 v8, v8, v10, v179
	v_max3_u32 v10, v25, v175, v173
	v_max3_u32 v9, v12, v9, v178
	v_max3_u32 v12, v26, v51, v174
	v_max3_u32 v3, v5, v4, v3
	v_max3_u32 v2, v27, v2, v176
	v_max_u32_e32 v4, v7, v16
	v_min_u32_e32 v5, v7, v16
	v_max_u32_e32 v7, v0, v17
	v_min_u32_e32 v0, v0, v17
	v_max_u32_e32 v16, v1, v8
	v_min_u32_e32 v1, v1, v8
	v_max_u32_e32 v8, v6, v10
	v_min_u32_e32 v6, v6, v10
	v_max_u32_e32 v10, v13, v9
	v_min_u32_e32 v9, v13, v9
	v_max_u32_e32 v13, v14, v12
	v_min_u32_e32 v12, v14, v12
	v_max_u32_e32 v14, v11, v3
	v_min_u32_e32 v3, v11, v3
	v_max_u32_e32 v11, v15, v2
	v_min_u32_e32 v2, v15, v2
	v_max_u32_e32 v15, v4, v10
	v_min_u32_e32 v4, v4, v10
	v_max_u32_e32 v10, v7, v13
	v_min_u32_e32 v7, v7, v13
	v_max_u32_e32 v13, v16, v14
	v_min_u32_e32 v14, v16, v14
	v_max_u32_e32 v16, v8, v11
	v_min_u32_e32 v8, v8, v11
	v_max_u32_e32 v11, v5, v9
	v_min_u32_e32 v5, v5, v9
	v_max_u32_e32 v9, v0, v12
	v_min_u32_e32 v0, v0, v12
	v_max_u32_e32 v12, v1, v3
	v_min_u32_e32 v1, v1, v3
	v_max_u32_e32 v3, v6, v2
	v_min_u32_e32 v2, v6, v2
	v_max_u32_e32 v6, v15, v13
	v_min_u32_e32 v13, v15, v13
	v_max_u32_e32 v15, v10, v16
	v_min_u32_e32 v10, v10, v16
	v_max_u32_e32 v16, v4, v14
	v_min_u32_e32 v4, v4, v14
	v_max_u32_e32 v14, v7, v8
	v_min_u32_e32 v7, v7, v8
	v_max_u32_e32 v8, v11, v12
	v_min_u32_e32 v11, v11, v12
	v_max_u32_e32 v12, v9, v3
	v_min_u32_e32 v3, v9, v3
	v_max_u32_e32 v9, v5, v1
	v_min_u32_e32 v1, v5, v1
	v_max_u32_e32 v5, v0, v2
	v_min_u32_e32 v0, v0, v2
	v_max_u32_e32 v2, v6, v15
	v_min_u32_e32 v6, v6, v15
	v_max_u32_e32 v15, v13, v10
	v_min_u32_e32 v10, v13, v10
	v_max_u32_e32 v13, v16, v14
	v_min_u32_e32 v14, v16, v14
	v_max_u32_e32 v16, v4, v7
	v_min_u32_e32 v4, v4, v7
	v_max_u32_e32 v7, v8, v12
	v_min_u32_e32 v8, v8, v12
	v_max_u32_e32 v12, v11, v3
	v_min_u32_e32 v3, v11, v3
	v_max_u32_e32 v11, v9, v5
	v_min_u32_e32 v5, v9, v5
	v_max_u32_e32 v9, v1, v0
	v_min_u32_e32 v0, v1, v0
	ds_bpermute_b32 v1, v55, v0
	ds_bpermute_b32 v17, v55, v9
	ds_bpermute_b32 v18, v55, v5
	ds_bpermute_b32 v19, v55, v11
	ds_bpermute_b32 v20, v55, v3
	ds_bpermute_b32 v21, v55, v12
	ds_bpermute_b32 v22, v55, v8
	ds_bpermute_b32 v23, v55, v7
	ds_bpermute_b32 v24, v55, v4
	ds_bpermute_b32 v25, v55, v16
	ds_bpermute_b32 v26, v55, v14
	ds_bpermute_b32 v27, v55, v13
	ds_bpermute_b32 v28, v55, v10
	ds_bpermute_b32 v29, v55, v15
	ds_bpermute_b32 v30, v55, v6
	ds_bpermute_b32 v31, v55, v2
	s_waitcnt lgkmcnt(14)
	v_max_u32_e32 v1, v2, v1
	v_max_u32_e32 v2, v6, v17
	s_waitcnt lgkmcnt(13)
	v_max_u32_e32 v6, v15, v18
	s_waitcnt lgkmcnt(12)
	v_max_u32_e32 v10, v10, v19
	s_waitcnt lgkmcnt(11)
	v_max_u32_e32 v13, v13, v20
	s_waitcnt lgkmcnt(10)
	v_max_u32_e32 v14, v14, v21
	s_waitcnt lgkmcnt(9)
	v_max_u32_e32 v15, v16, v22
	s_waitcnt lgkmcnt(8)
	v_max_u32_e32 v4, v4, v23
	s_waitcnt lgkmcnt(7)
	v_max_u32_e32 v7, v7, v24
	s_waitcnt lgkmcnt(6)
	v_max_u32_e32 v8, v8, v25
	s_waitcnt lgkmcnt(5)
	v_max_u32_e32 v12, v12, v26
	s_waitcnt lgkmcnt(4)
	v_max_u32_e32 v3, v3, v27
	s_waitcnt lgkmcnt(3)
	v_max_u32_e32 v11, v11, v28
	s_waitcnt lgkmcnt(2)
	v_max_u32_e32 v5, v5, v29
	s_waitcnt lgkmcnt(1)
	v_max_u32_e32 v9, v9, v30
	s_waitcnt lgkmcnt(0)
	v_max_u32_e32 v0, v0, v31
	v_max_u32_e32 v16, v1, v7
	v_min_u32_e32 v1, v1, v7
	v_max_u32_e32 v7, v2, v8
	v_min_u32_e32 v2, v2, v8
	v_max_u32_e32 v8, v6, v12
	v_min_u32_e32 v6, v6, v12
	v_max_u32_e32 v12, v10, v3
	v_min_u32_e32 v3, v10, v3
	v_max_u32_e32 v10, v13, v11
	v_min_u32_e32 v11, v13, v11
	v_max_u32_e32 v13, v14, v5
	v_min_u32_e32 v5, v14, v5
	v_max_u32_e32 v14, v15, v9
	v_min_u32_e32 v9, v15, v9
	v_max_u32_e32 v15, v4, v0
	v_min_u32_e32 v0, v4, v0
	v_max_u32_e32 v4, v16, v10
	v_min_u32_e32 v10, v16, v10
	v_max_u32_e32 v16, v7, v13
	v_min_u32_e32 v7, v7, v13
	v_max_u32_e32 v13, v8, v14
	v_min_u32_e32 v8, v8, v14
	v_max_u32_e32 v14, v12, v15
	v_min_u32_e32 v12, v12, v15
	v_max_u32_e32 v15, v1, v11
	v_min_u32_e32 v1, v1, v11
	v_max_u32_e32 v11, v2, v5
	v_min_u32_e32 v2, v2, v5
	v_max_u32_e32 v5, v6, v9
	v_min_u32_e32 v6, v6, v9
	v_max_u32_e32 v9, v3, v0
	v_min_u32_e32 v0, v3, v0
	v_max_u32_e32 v3, v4, v13
	v_min_u32_e32 v4, v4, v13
	v_max_u32_e32 v13, v16, v14
	v_min_u32_e32 v14, v16, v14
	v_max_u32_e32 v16, v10, v8
	v_min_u32_e32 v8, v10, v8
	v_max_u32_e32 v10, v7, v12
	v_min_u32_e32 v7, v7, v12
	v_max_u32_e32 v12, v15, v5
	v_min_u32_e32 v5, v15, v5
	v_max_u32_e32 v15, v11, v9
	v_min_u32_e32 v9, v11, v9
	v_max_u32_e32 v11, v1, v6
	v_min_u32_e32 v1, v1, v6
	v_max_u32_e32 v6, v2, v0
	v_min_u32_e32 v0, v2, v0
	v_max_u32_e32 v2, v3, v13
	v_min_u32_e32 v3, v3, v13
	v_max_u32_e32 v13, v4, v14
	v_min_u32_e32 v4, v4, v14
	v_max_u32_e32 v14, v16, v10
	v_min_u32_e32 v10, v16, v10
	v_max_u32_e32 v16, v8, v7
	v_min_u32_e32 v7, v8, v7
	v_max_u32_e32 v8, v12, v15
	v_min_u32_e32 v12, v12, v15
	v_max_u32_e32 v15, v5, v9
	v_min_u32_e32 v5, v5, v9
	v_max_u32_e32 v9, v11, v6
	v_min_u32_e32 v6, v11, v6
	v_max_u32_e32 v11, v1, v0
	v_min_u32_e32 v0, v1, v0
	ds_bpermute_b32 v1, v56, v0
	ds_bpermute_b32 v17, v56, v11
	ds_bpermute_b32 v18, v56, v6
	ds_bpermute_b32 v19, v56, v9
	ds_bpermute_b32 v20, v56, v5
	ds_bpermute_b32 v21, v56, v15
	ds_bpermute_b32 v22, v56, v12
	ds_bpermute_b32 v23, v56, v8
	ds_bpermute_b32 v24, v56, v7
	ds_bpermute_b32 v25, v56, v16
	ds_bpermute_b32 v26, v56, v10
	ds_bpermute_b32 v27, v56, v14
	ds_bpermute_b32 v28, v56, v4
	ds_bpermute_b32 v29, v56, v13
	ds_bpermute_b32 v30, v56, v3
	ds_bpermute_b32 v31, v56, v2
	s_waitcnt lgkmcnt(14)
	v_max_u32_e32 v1, v2, v1
	v_max_u32_e32 v2, v3, v17
	s_waitcnt lgkmcnt(13)
	v_max_u32_e32 v3, v13, v18
	s_waitcnt lgkmcnt(12)
	v_max_u32_e32 v4, v4, v19
	s_waitcnt lgkmcnt(11)
	v_max_u32_e32 v13, v14, v20
	s_waitcnt lgkmcnt(10)
	v_max_u32_e32 v10, v10, v21
	s_waitcnt lgkmcnt(9)
	v_max_u32_e32 v14, v16, v22
	s_waitcnt lgkmcnt(8)
	v_max_u32_e32 v7, v7, v23
	s_waitcnt lgkmcnt(7)
	v_max_u32_e32 v8, v8, v24
	s_waitcnt lgkmcnt(6)
	v_max_u32_e32 v12, v12, v25
	s_waitcnt lgkmcnt(5)
	v_max_u32_e32 v15, v15, v26
	s_waitcnt lgkmcnt(4)
	v_max_u32_e32 v5, v5, v27
	s_waitcnt lgkmcnt(3)
	v_max_u32_e32 v9, v9, v28
	s_waitcnt lgkmcnt(2)
	v_max_u32_e32 v6, v6, v29
	s_waitcnt lgkmcnt(1)
	v_max_u32_e32 v11, v11, v30
	s_waitcnt lgkmcnt(0)
	v_max_u32_e32 v0, v0, v31
	v_max_u32_e32 v16, v1, v8
	v_min_u32_e32 v1, v1, v8
	v_max_u32_e32 v8, v2, v12
	v_min_u32_e32 v2, v2, v12
	v_max_u32_e32 v12, v3, v15
	v_min_u32_e32 v3, v3, v15
	v_max_u32_e32 v15, v4, v5
	v_min_u32_e32 v4, v4, v5
	v_max_u32_e32 v5, v13, v9
	v_min_u32_e32 v9, v13, v9
	v_max_u32_e32 v13, v10, v6
	v_min_u32_e32 v6, v10, v6
	v_max_u32_e32 v10, v14, v11
	v_min_u32_e32 v11, v14, v11
	v_max_u32_e32 v14, v7, v0
	v_min_u32_e32 v0, v7, v0
	v_max_u32_e32 v7, v16, v5
	v_min_u32_e32 v5, v16, v5
	v_max_u32_e32 v16, v8, v13
	v_min_u32_e32 v8, v8, v13
	v_max_u32_e32 v13, v12, v10
	v_min_u32_e32 v10, v12, v10
	v_max_u32_e32 v12, v15, v14
	v_min_u32_e32 v14, v15, v14
	v_max_u32_e32 v15, v1, v9
	v_min_u32_e32 v1, v1, v9
	v_max_u32_e32 v9, v2, v6
	v_min_u32_e32 v2, v2, v6
	v_max_u32_e32 v6, v3, v11
	v_min_u32_e32 v3, v3, v11
	v_max_u32_e32 v11, v4, v0
	v_min_u32_e32 v0, v4, v0
	v_max_u32_e32 v4, v7, v13
	v_min_u32_e32 v13, v7, v13
	v_max_u32_e32 v7, v16, v12
	v_min_u32_e32 v12, v16, v12
	v_max_u32_e32 v16, v5, v10
	v_min_u32_e32 v10, v5, v10
	v_max_u32_e32 v17, v8, v14
	v_min_u32_e32 v18, v8, v14
	v_max_u32_e32 v19, v15, v6
	v_min_u32_e32 v20, v15, v6
	v_max_u32_e32 v21, v9, v11
	v_min_u32_e32 v9, v9, v11
	v_max_u32_e32 v11, v1, v3
	v_min_u32_e32 v1, v1, v3
	v_max_u32_e32 v22, v2, v0
	v_min_u32_e32 v0, v2, v0
	v_max_u32_e32 v3, v4, v7
	v_min_u32_e32 v6, v4, v7
	v_max_u32_e32 v7, v13, v12
	v_min_u32_e32 v5, v13, v12
	v_max_u32_e32 v8, v16, v17
	v_min_u32_e32 v13, v16, v17
	v_max_u32_e32 v14, v10, v18
	v_min_u32_e32 v16, v10, v18
	v_max_u32_e32 v15, v19, v21
	v_min_u32_e32 v17, v19, v21
	v_max_u32_e32 v18, v20, v9
	v_min_u32_e32 v19, v20, v9
	v_max_u32_e32 v9, v11, v22
	v_min_u32_e32 v10, v11, v22
	v_max_u32_e32 v11, v1, v0
	v_min_u32_e32 v12, v1, v0
	v_cndmask_b32_e64 v0, v163, v166, s[10:11]
	v_cndmask_b32_e64 v1, v171, v158, s[10:11]
	v_cndmask_b32_e64 v0, v1, v0, s[12:13]
	v_cndmask_b32_e64 v1, v160, v165, s[10:11]
	v_cndmask_b32_e64 v2, v172, v159, s[10:11]
	v_cndmask_b32_e64 v1, v2, v1, s[12:13]
	v_bitop3_b32 v21, v1, s24, v1 bitop3:0xc
	v_cndmask_b32_e64 v1, v161, v164, s[10:11]
	v_cndmask_b32_e64 v2, v167, v169, s[10:11]
	v_cndmask_b32_e64 v1, v2, v1, s[12:13]
	v_bitop3_b32 v22, v1, s24, v1 bitop3:0xc
	v_cndmask_b32_e64 v1, v157, v162, s[10:11]
	v_cndmask_b32_e64 v2, v168, v170, s[10:11]
	v_cndmask_b32_e64 v1, v2, v1, s[12:13]
	v_bitop3_b32 v23, v1, s24, v1 bitop3:0xc
	v_cndmask_b32_e64 v1, v8, v3, s[10:11]
	v_cndmask_b32_e64 v2, v9, v15, s[10:11]
	v_bitop3_b32 v20, v0, s24, v0 bitop3:0xc
	v_add_u32_e32 v0, v57, v32
	v_cndmask_b32_e64 v1, v2, v1, s[12:13]
	ds_write_b128 v0, v[20:23]
	v_bitop3_b32 v20, v1, s24, v1 bitop3:0xc
	v_cndmask_b32_e64 v1, v13, v6, s[10:11]
	v_cndmask_b32_e64 v2, v10, v17, s[10:11]
	v_cndmask_b32_e64 v1, v2, v1, s[12:13]
	v_bitop3_b32 v21, v1, s24, v1 bitop3:0xc
	v_cndmask_b32_e64 v1, v14, v7, s[10:11]
	v_cndmask_b32_e64 v2, v11, v18, s[10:11]
	v_cndmask_b32_e64 v1, v2, v1, s[12:13]
	v_bitop3_b32 v22, v1, s24, v1 bitop3:0xc
	v_cndmask_b32_e64 v1, v16, v5, s[10:11]
	v_cndmask_b32_e64 v2, v12, v19, s[10:11]
	v_cndmask_b32_e64 v1, v2, v1, s[12:13]
	v_bitop3_b32 v23, v1, s24, v1 bitop3:0xc
	ds_write_b128 v0, v[20:23] offset:64
	v_cndmask_b32_e64 v0, v170, v169, s[10:11]
	v_cndmask_b32_e64 v1, v172, v171, s[10:11]
	v_cndmask_b32_e64 v0, v1, v0, s[12:13]
	v_cmp_gt_i32_e32 vcc, 0, v0
	v_and_b32_e32 v2, 0x7fffff80, v0
	v_and_b32_e32 v4, 0xffffff80, v3
	v_and_b32_e32 v0, 0xffffff80, v0
	v_cmp_gt_i32_e64 s[0:1], 0, v3
	v_and_b32_e32 v1, 0x7fffff80, v3
	v_xor_b32_e32 v4, -1, v4
	v_xor_b32_e32 v0, -1, v0
	v_cndmask_b32_e64 v1, v4, v1, s[0:1]
	v_cndmask_b32_e32 v0, v0, v2, vcc
	v_mov_b32_e32 v2, 0
	v_mov_b32_e32 v4, 0
	s_and_saveexec_b64 s[0:1], s[16:17]
	s_cbranch_execz .LBB0_1369
	v_cndmask_b32_e64 v4, v168, v167, s[10:11]
	v_cndmask_b32_e64 v4, v166, v4, s[12:13]
	v_and_b32_e32 v20, 0x7fffff80, v4
	v_bitop3_b32 v21, v4, s24, v4 bitop3:0xcf
	v_cmp_gt_i32_e32 vcc, 0, v4
	s_nop 1
	v_cndmask_b32_e32 v4, v21, v20, vcc
	v_add_f32_e32 v4, v1, v4
	v_not_b32_e32 v20, v4
	v_or_b32_e32 v21, 0x80000000, v4
	v_cmp_gt_i32_e32 vcc, 0, v4
	s_nop 1
	v_cndmask_b32_e32 v4, v21, v20, vcc
	v_and_b32_e32 v4, 0xffffffc0, v4
	v_bitop3_b32 v4, v53, 15, v4 bitop3:0x36
